# all softmax VALU inside MFMA gaps: half of the exp/cvt in the next tile's QK^T gaps, the other cvt in the second half of P.V (no VALU-only tail)
# speedup vs baseline: 1.0015x; 1.0015x over previous
; #define SBAR() __builtin_amdgcn_sched_barrier(0)
; __device__ __forceinline__ void qkt(f32x16& p0, f32x16& p1, const bf16_t* Ks, const bf16x8* qr, int r32, int hi) {
;   p0 = f32x16{}; p1 = f32x16{};
;   for (int d0 = 0; d0 < 8; ++d0) { int cb = (d0 * 16 + hi * 8) * 2;
;     bf16x8 b0 = *reinterpret_cast<const bf16x8*>((const char*)Ks + KSWZ(r32, cb));
;     bf16x8 b1 = *reinterpret_cast<const bf16x8*>((const char*)Ks + KSWZ(32 + r32, cb));
;     p0 = __builtin_amdgcn_mfma_f32_32x32x16_bf16(b0, qr[d0], p0, 0, 0, 0);
;     p1 = __builtin_amdgcn_mfma_f32_32x32x16_bf16(b1, qr[d0], p1, 0, 0, 0); }
; }
; template <int D0> __device__ __forceinline__ void pv_rd(s16x4 (&r)[8], int vb) {
;   r[0] = tr_read<v_rd_off(D0, 0, 0)>(vb); r[1] = tr_read<v_rd_off(D0, 0, 1)>(vb); r[2] = tr_read<v_rd_off(D0, 1, 0)>(vb); r[3] = tr_read<v_rd_off(D0, 1, 1)>(vb);
;   r[4] = tr_read<v_rd_off(D0, 2, 0)>(vb); r[5] = tr_read<v_rd_off(D0, 2, 1)>(vb); r[6] = tr_read<v_rd_off(D0, 3, 0)>(vb); r[7] = tr_read<v_rd_off(D0, 3, 1)>(vb);
; }
; __device__ __forceinline__ void pv_mm(f32x16& od, const s16x4 (&r)[8], bf16x8 pa0, bf16x8 pa1, bf16x8 pa2, bf16x8 pa3) {
;     ...
;   od = __builtin_amdgcn_mfma_f32_32x32x16_bf16(pa0, PK(r[0], r[1]), od, 0, 0, 0);
;   od = __builtin_amdgcn_mfma_f32_32x32x16_bf16(pa1, PK(r[2], r[3]), od, 0, 0, 0);
;   od = __builtin_amdgcn_mfma_f32_32x32x16_bf16(pa2, PK(r[4], r[5]), od, 0, 0, 0);
;   od = __builtin_amdgcn_mfma_f32_32x32x16_bf16(pa3, PK(r[6], r[7]), od, 0, 0, 0);
;     ...
; }
; __device__ __forceinline__ void pv_d0(f32x16* o, int vb, bf16x8 pa0, bf16x8 pa1, bf16x8 pa2, bf16x8 pa3) {
;   s16x4 ra[8], rb[8];
;   pv_rd<0>(ra, vb); pv_rd<1>(rb, vb);
;   asm volatile("s_waitcnt lgkmcnt(8)" ::: "memory"); SBAR(); pv_mm(o[0], ra, pa0, pa1, pa2, pa3); pv_rd<2>(ra, vb);
;   asm volatile("s_waitcnt lgkmcnt(8)" ::: "memory"); SBAR(); pv_mm(o[1], rb, pa0, pa1, pa2, pa3); pv_rd<3>(rb, vb);
;   asm volatile("s_waitcnt lgkmcnt(8)" ::: "memory"); SBAR(); pv_mm(o[2], ra, pa0, pa1, pa2, pa3);
;   asm volatile("s_waitcnt lgkmcnt(0)" ::: "memory"); SBAR(); pv_mm(o[3], rb, pa0, pa1, pa2, pa3);
; }
.Lf16_se_N0:
	s_waitcnt lgkmcnt(8)
	v_mfma_f32_16x16x32_bf16 v[2:5], v[214:217], v[130:133], v[2:5]
	v_mfma_f32_16x16x32_bf16 v[6:9], v[214:217], v[138:141], v[6:9]
	v_exp_f32_e32 v66, v66
	v_mfma_f32_16x16x32_bf16 v[10:13], v[218:221], v[130:133], v[10:13]
	v_mfma_f32_16x16x32_bf16 v[14:17], v[218:221], v[138:141], v[14:17]
	v_exp_f32_e32 v67, v67
	ds_read_b64_tr_b16 v[238:239], v191 offset:1536
	ds_read_b64_tr_b16 v[240:241], v191 offset:5632
	ds_read_b64_tr_b16 v[242:243], v192 offset:1536
	ds_read_b64_tr_b16 v[244:245], v192 offset:5632
	s_waitcnt lgkmcnt(8)
	v_mfma_f32_16x16x32_bf16 v[18:21], v[222:225], v[130:133], v[18:21]
	v_mfma_f32_16x16x32_bf16 v[22:25], v[222:225], v[138:141], v[22:25]
	v_exp_f32_e32 v68, v68
	v_mfma_f32_16x16x32_bf16 v[26:29], v[226:229], v[130:133], v[26:29]
	v_mfma_f32_16x16x32_bf16 v[30:33], v[226:229], v[138:141], v[30:33]
	v_exp_f32_e32 v69, v69
	v_mfma_f32_16x16x32_bf16 v[246:249], v[194:197], v[130:133], v[246:249]
	ds_read_b64_tr_b16 v[214:215], v191 offset:8192
	ds_read_b64_tr_b16 v[216:217], v191 offset:12288
	ds_read_b64_tr_b16 v[218:219], v192 offset:8192
	ds_read_b64_tr_b16 v[220:221], v192 offset:12288
	s_waitcnt lgkmcnt(8)
	v_mfma_f32_16x16x32_bf16 v[34:37], v[230:233], v[130:133], v[34:37]
	v_mfma_f32_16x16x32_bf16 v[38:41], v[230:233], v[138:141], v[38:41]
	v_exp_f32_e32 v70, v70
	v_mfma_f32_16x16x32_bf16 v[42:45], v[234:237], v[130:133], v[42:45]
	v_mfma_f32_16x16x32_bf16 v[46:49], v[234:237], v[138:141], v[46:49]
	v_exp_f32_e32 v71, v71
	ds_read_b64_tr_b16 v[222:223], v191 offset:8704
	ds_read_b64_tr_b16 v[224:225], v191 offset:12800
	ds_read_b64_tr_b16 v[226:227], v192 offset:8704
	ds_read_b64_tr_b16 v[228:229], v192 offset:12800
	s_waitcnt lgkmcnt(8)
	v_mfma_f32_16x16x32_bf16 v[50:53], v[238:241], v[130:133], v[50:53]
	v_mfma_f32_16x16x32_bf16 v[54:57], v[238:241], v[138:141], v[54:57]
	v_exp_f32_e32 v72, v72
	v_mfma_f32_16x16x32_bf16 v[58:61], v[242:245], v[130:133], v[58:61]
	v_mfma_f32_16x16x32_bf16 v[62:65], v[242:245], v[138:141], v[62:65]
	v_exp_f32_e32 v73, v73
	v_mfma_f32_16x16x32_bf16 v[252:255], v[194:197], v[138:141], v[252:255]
	ds_read_b64_tr_b16 v[230:231], v191 offset:9216
	ds_read_b64_tr_b16 v[232:233], v191 offset:13312
	ds_read_b64_tr_b16 v[234:235], v192 offset:9216
	ds_read_b64_tr_b16 v[236:237], v192 offset:13312
	s_waitcnt lgkmcnt(8)
	v_mfma_f32_16x16x32_bf16 v[2:5], v[214:217], v[134:137], v[2:5]
	v_exp_f32_e32 v74, v74
	v_mfma_f32_16x16x32_bf16 v[6:9], v[214:217], v[142:145], v[6:9]
	v_cvt_pk_bf16_f32 v130, v66, v67
	v_mfma_f32_16x16x32_bf16 v[10:13], v[218:221], v[134:137], v[10:13]
	v_exp_f32_e32 v75, v75
	v_mfma_f32_16x16x32_bf16 v[14:17], v[218:221], v[142:145], v[14:17]
	v_cvt_pk_bf16_f32 v131, v68, v69
	ds_read_b64_tr_b16 v[238:239], v191 offset:9728
	ds_read_b64_tr_b16 v[240:241], v191 offset:13824
	ds_read_b64_tr_b16 v[242:243], v192 offset:9728
	ds_read_b64_tr_b16 v[244:245], v192 offset:13824
	s_waitcnt lgkmcnt(8)
	v_mfma_f32_16x16x32_bf16 v[18:21], v[222:225], v[134:137], v[18:21]
	v_exp_f32_e32 v76, v76
	v_mfma_f32_16x16x32_bf16 v[22:25], v[222:225], v[142:145], v[22:25]
	v_cvt_pk_bf16_f32 v132, v74, v75
	v_mfma_f32_16x16x32_bf16 v[26:29], v[226:229], v[134:137], v[26:29]
	v_exp_f32_e32 v77, v77
	v_mfma_f32_16x16x32_bf16 v[30:33], v[226:229], v[142:145], v[30:33]
	v_cvt_pk_bf16_f32 v133, v76, v77
	v_mfma_f32_16x16x32_bf16 v[246:249], v[194:197], v[134:137], v[246:249]
	s_waitcnt lgkmcnt(4)
	v_mfma_f32_16x16x32_bf16 v[34:37], v[230:233], v[134:137], v[34:37]
	v_exp_f32_e32 v78, v78
	v_mfma_f32_16x16x32_bf16 v[38:41], v[230:233], v[142:145], v[38:41]
	v_cvt_pk_bf16_f32 v138, v70, v71
	v_mfma_f32_16x16x32_bf16 v[42:45], v[234:237], v[134:137], v[42:45]
	v_exp_f32_e32 v79, v79
	v_mfma_f32_16x16x32_bf16 v[46:49], v[234:237], v[142:145], v[46:49]
	v_cvt_pk_bf16_f32 v139, v72, v73
	s_waitcnt lgkmcnt(0)
	v_mfma_f32_16x16x32_bf16 v[50:53], v[238:241], v[134:137], v[50:53]
	v_exp_f32_e32 v80, v80
	v_mfma_f32_16x16x32_bf16 v[54:57], v[238:241], v[142:145], v[54:57]
	v_cvt_pk_bf16_f32 v140, v78, v79
	v_mfma_f32_16x16x32_bf16 v[58:61], v[242:245], v[134:137], v[58:61]
	v_exp_f32_e32 v81, v81
	v_mfma_f32_16x16x32_bf16 v[62:65], v[242:245], v[142:145], v[62:65]
	v_cvt_pk_bf16_f32 v141, v80, v81
	v_mfma_f32_16x16x32_bf16 v[252:255], v[194:197], v[142:145], v[252:255]
	s_add_i32 s97, s97, 1
	ds_read_b128 v[146:149], v187 offset:0
	ds_read_b128 v[150:153], v188 offset:0
	ds_read_b128 v[154:157], v189 offset:0
	ds_read_b128 v[158:161], v190 offset:0
	ds_read_b128 v[198:201], v187 offset:4096
	ds_read_b128 v[202:205], v188 offset:4096
	ds_read_b128 v[206:209], v189 offset:4096
	ds_read_b128 v[210:213], v190 offset:4096
	s_waitcnt lgkmcnt(6)
	v_mfma_f32_16x16x32_bf16 v[66:69], v[146:149], v[98:101], 0
	v_exp_f32_e32 v82, v82
	v_mfma_f32_16x16x32_bf16 v[70:73], v[146:149], v[114:117], 0
	v_exp_f32_e32 v83, v83
	v_mfma_f32_16x16x32_bf16 v[66:69], v[150:153], v[102:105], v[66:69]
	v_exp_f32_e32 v84, v84
	v_mfma_f32_16x16x32_bf16 v[70:73], v[150:153], v[118:121], v[70:73]
	v_exp_f32_e32 v85, v85
	ds_read_b128 v[146:149], v187 offset:8192
	ds_read_b128 v[150:153], v188 offset:8192
	s_waitcnt lgkmcnt(6)
	v_mfma_f32_16x16x32_bf16 v[66:69], v[154:157], v[106:109], v[66:69]
	v_exp_f32_e32 v86, v86
	v_mfma_f32_16x16x32_bf16 v[70:73], v[154:157], v[122:125], v[70:73]
	v_exp_f32_e32 v87, v87
	v_mfma_f32_16x16x32_bf16 v[66:69], v[158:161], v[110:113], v[66:69]
	v_exp_f32_e32 v88, v88
	v_mfma_f32_16x16x32_bf16 v[70:73], v[158:161], v[126:129], v[70:73]
	v_exp_f32_e32 v89, v89
	ds_read_b128 v[154:157], v189 offset:8192
	ds_read_b128 v[158:161], v190 offset:8192
	s_waitcnt lgkmcnt(6)
; #define SBAR() __builtin_amdgcn_sched_barrier(0)
; __device__ __forceinline__ void qkt(f32x16& p0, f32x16& p1, const bf16_t* Ks, const bf16x8* qr, int r32, int hi) {
;   p0 = f32x16{}; p1 = f32x16{};
;   for (int d0 = 0; d0 < 8; ++d0) { int cb = (d0 * 16 + hi * 8) * 2;
;     bf16x8 b0 = *reinterpret_cast<const bf16x8*>((const char*)Ks + KSWZ(r32, cb));
;     bf16x8 b1 = *reinterpret_cast<const bf16x8*>((const char*)Ks + KSWZ(32 + r32, cb));
;     p0 = __builtin_amdgcn_mfma_f32_32x32x16_bf16(b0, qr[d0], p0, 0, 0, 0);
;     p1 = __builtin_amdgcn_mfma_f32_32x32x16_bf16(b1, qr[d0], p1, 0, 0, 0); }
; }
; template <int D0> __device__ __forceinline__ void pv_rd(s16x4 (&r)[8], int vb) {
;   r[0] = tr_read<v_rd_off(D0, 0, 0)>(vb); r[1] = tr_read<v_rd_off(D0, 0, 1)>(vb); r[2] = tr_read<v_rd_off(D0, 1, 0)>(vb); r[3] = tr_read<v_rd_off(D0, 1, 1)>(vb);
;   r[4] = tr_read<v_rd_off(D0, 2, 0)>(vb); r[5] = tr_read<v_rd_off(D0, 2, 1)>(vb); r[6] = tr_read<v_rd_off(D0, 3, 0)>(vb); r[7] = tr_read<v_rd_off(D0, 3, 1)>(vb);
; }
; __device__ __forceinline__ void pv_mm(f32x16& od, const s16x4 (&r)[8], bf16x8 pa0, bf16x8 pa1, bf16x8 pa2, bf16x8 pa3) {
;     ...
;   od = __builtin_amdgcn_mfma_f32_32x32x16_bf16(pa0, PK(r[0], r[1]), od, 0, 0, 0);
;   od = __builtin_amdgcn_mfma_f32_32x32x16_bf16(pa1, PK(r[2], r[3]), od, 0, 0, 0);
;   od = __builtin_amdgcn_mfma_f32_32x32x16_bf16(pa2, PK(r[4], r[5]), od, 0, 0, 0);
;   od = __builtin_amdgcn_mfma_f32_32x32x16_bf16(pa3, PK(r[6], r[7]), od, 0, 0, 0);
;     ...
; }
; __device__ __forceinline__ void pv_d0(f32x16* o, int vb, bf16x8 pa0, bf16x8 pa1, bf16x8 pa2, bf16x8 pa3) {
;   s16x4 ra[8], rb[8];
;   pv_rd<0>(ra, vb); pv_rd<1>(rb, vb);
;   asm volatile("s_waitcnt lgkmcnt(8)" ::: "memory"); SBAR(); pv_mm(o[0], ra, pa0, pa1, pa2, pa3); pv_rd<2>(ra, vb);
;   asm volatile("s_waitcnt lgkmcnt(8)" ::: "memory"); SBAR(); pv_mm(o[1], rb, pa0, pa1, pa2, pa3); pv_rd<3>(rb, vb);
;   asm volatile("s_waitcnt lgkmcnt(8)" ::: "memory"); SBAR(); pv_mm(o[2], ra, pa0, pa1, pa2, pa3);
;   asm volatile("s_waitcnt lgkmcnt(0)" ::: "memory"); SBAR(); pv_mm(o[3], rb, pa0, pa1, pa2, pa3);
; }
	v_mfma_f32_16x16x32_bf16 v[74:77], v[198:201], v[98:101], 0
	v_exp_f32_e32 v90, v90
	v_mfma_f32_16x16x32_bf16 v[78:81], v[198:201], v[114:117], 0
	v_exp_f32_e32 v91, v91
	v_cvt_pk_bf16_f32 v134, v82, v83
	v_mfma_f32_16x16x32_bf16 v[74:77], v[202:205], v[102:105], v[74:77]
	v_exp_f32_e32 v92, v92
	v_cvt_pk_bf16_f32 v135, v84, v85
	v_mfma_f32_16x16x32_bf16 v[78:81], v[202:205], v[118:121], v[78:81]
	v_exp_f32_e32 v93, v93
	v_cvt_pk_bf16_f32 v142, v86, v87
	ds_read_b128 v[198:201], v187 offset:12288
	ds_read_b128 v[202:205], v188 offset:12288
	s_waitcnt lgkmcnt(6)
	v_mfma_f32_16x16x32_bf16 v[74:77], v[206:209], v[106:109], v[74:77]
	v_exp_f32_e32 v94, v94
	v_cvt_pk_bf16_f32 v143, v88, v89
	v_mfma_f32_16x16x32_bf16 v[78:81], v[206:209], v[122:125], v[78:81]
	v_exp_f32_e32 v95, v95
	v_mfma_f32_16x16x32_bf16 v[74:77], v[210:213], v[110:113], v[74:77]
	v_exp_f32_e32 v96, v96
	v_mfma_f32_16x16x32_bf16 v[78:81], v[210:213], v[126:129], v[78:81]
	v_exp_f32_e32 v97, v97
	ds_read_b128 v[206:209], v189 offset:12288
	ds_read_b128 v[210:213], v190 offset:12288
	s_waitcnt lgkmcnt(6)
	v_mfma_f32_16x16x32_bf16 v[82:85], v[146:149], v[98:101], 0
	v_mfma_f32_16x16x32_bf16 v[86:89], v[146:149], v[114:117], 0
	v_cvt_pk_bf16_f32 v136, v90, v91
	v_mfma_f32_16x16x32_bf16 v[82:85], v[150:153], v[102:105], v[82:85]
	v_cvt_pk_bf16_f32 v137, v92, v93
	v_mfma_f32_16x16x32_bf16 v[86:89], v[150:153], v[118:121], v[86:89]
	v_cvt_pk_bf16_f32 v144, v94, v95
	s_waitcnt lgkmcnt(4)
	v_mfma_f32_16x16x32_bf16 v[82:85], v[154:157], v[106:109], v[82:85]
	v_cvt_pk_bf16_f32 v145, v96, v97
	v_mfma_f32_16x16x32_bf16 v[86:89], v[154:157], v[122:125], v[86:89]
	v_mfma_f32_16x16x32_bf16 v[82:85], v[158:161], v[110:113], v[82:85]
	v_mfma_f32_16x16x32_bf16 v[86:89], v[158:161], v[126:129], v[86:89]
	s_waitcnt lgkmcnt(2)
	v_mfma_f32_16x16x32_bf16 v[90:93], v[198:201], v[98:101], 0
	v_mfma_f32_16x16x32_bf16 v[94:97], v[198:201], v[114:117], 0
	v_mfma_f32_16x16x32_bf16 v[90:93], v[202:205], v[102:105], v[90:93]
	v_mfma_f32_16x16x32_bf16 v[94:97], v[202:205], v[118:121], v[94:97]
	ds_read_b64_tr_b16 v[214:215], v191 offset:32768
	ds_read_b64_tr_b16 v[216:217], v191 offset:36864
	ds_read_b64_tr_b16 v[218:219], v192 offset:32768
	ds_read_b64_tr_b16 v[220:221], v192 offset:36864
	ds_read_b64_tr_b16 v[222:223], v191 offset:33280
	ds_read_b64_tr_b16 v[224:225], v191 offset:37376
	ds_read_b64_tr_b16 v[226:227], v192 offset:33280
	ds_read_b64_tr_b16 v[228:229], v192 offset:37376
	ds_read_b64_tr_b16 v[230:231], v191 offset:33792
	ds_read_b64_tr_b16 v[232:233], v191 offset:37888
	ds_read_b64_tr_b16 v[234:235], v192 offset:33792
	ds_read_b64_tr_b16 v[236:237], v192 offset:37888
	s_waitcnt lgkmcnt(12)
	v_mfma_f32_16x16x32_bf16 v[90:93], v[206:209], v[106:109], v[90:93]
	v_mfma_f32_16x16x32_bf16 v[94:97], v[206:209], v[122:125], v[94:97]
	v_mfma_f32_16x16x32_bf16 v[90:93], v[210:213], v[110:113], v[90:93]
	v_mfma_f32_16x16x32_bf16 v[94:97], v[210:213], v[126:129], v[94:97]
	s_waitcnt vmcnt(0) lgkmcnt(0)
	s_barrier
	s_cmp_ge_u32 s97, 130
	s_cbranch_scc1 .Lf16_se_N1
	s_add_i32 m0, s96, 0x0
	s_nop 0
	global_load_lds_dwordx4 v170, s[2:3]
	s_add_i32 m0, s96, 0x2000
	s_nop 0
	global_load_lds_dwordx4 v172, s[2:3]
	s_add_i32 m0, s96, 0x4000
	s_nop 0
	global_load_lds_dwordx4 v171, s[2:3]
	s_add_i32 m0, s96, 0x6000
	s_nop 0
	global_load_lds_dwordx4 v173, s[2:3]
	s_add_u32 s2, s2, 0x4000
	s_addc_u32 s3, s3, 0
.Lf16_se_N1:
	s_waitcnt lgkmcnt(8)
	v_mfma_f32_16x16x32_bf16 v[2:5], v[214:217], v[130:133], v[2:5]
	v_mfma_f32_16x16x32_bf16 v[6:9], v[214:217], v[138:141], v[6:9]
	v_exp_f32_e32 v66, v66
	v_mfma_f32_16x16x32_bf16 v[10:13], v[218:221], v[130:133], v[10:13]
	v_mfma_f32_16x16x32_bf16 v[14:17], v[218:221], v[138:141], v[14:17]
	v_exp_f32_e32 v67, v67
	ds_read_b64_tr_b16 v[238:239], v191 offset:34304
	ds_read_b64_tr_b16 v[240:241], v191 offset:38400
	ds_read_b64_tr_b16 v[242:243], v192 offset:34304
	ds_read_b64_tr_b16 v[244:245], v192 offset:38400
	s_waitcnt lgkmcnt(8)
	v_mfma_f32_16x16x32_bf16 v[18:21], v[222:225], v[130:133], v[18:21]
	v_mfma_f32_16x16x32_bf16 v[22:25], v[222:225], v[138:141], v[22:25]
	v_exp_f32_e32 v68, v68
	v_mfma_f32_16x16x32_bf16 v[26:29], v[226:229], v[130:133], v[26:29]
	v_mfma_f32_16x16x32_bf16 v[30:33], v[226:229], v[138:141], v[30:33]
	v_exp_f32_e32 v69, v69
	v_mfma_f32_16x16x32_bf16 v[246:249], v[194:197], v[130:133], v[246:249]
	ds_read_b64_tr_b16 v[214:215], v191 offset:40960
	ds_read_b64_tr_b16 v[216:217], v191 offset:45056
	ds_read_b64_tr_b16 v[218:219], v192 offset:40960
	ds_read_b64_tr_b16 v[220:221], v192 offset:45056
	s_waitcnt lgkmcnt(8)
	v_mfma_f32_16x16x32_bf16 v[34:37], v[230:233], v[130:133], v[34:37]
	v_mfma_f32_16x16x32_bf16 v[38:41], v[230:233], v[138:141], v[38:41]
	v_exp_f32_e32 v70, v70
	v_mfma_f32_16x16x32_bf16 v[42:45], v[234:237], v[130:133], v[42:45]
	v_mfma_f32_16x16x32_bf16 v[46:49], v[234:237], v[138:141], v[46:49]
	v_exp_f32_e32 v71, v71
	ds_read_b64_tr_b16 v[222:223], v191 offset:41472
	ds_read_b64_tr_b16 v[224:225], v191 offset:45568
	ds_read_b64_tr_b16 v[226:227], v192 offset:41472
	ds_read_b64_tr_b16 v[228:229], v192 offset:45568
	s_waitcnt lgkmcnt(8)
	v_mfma_f32_16x16x32_bf16 v[50:53], v[238:241], v[130:133], v[50:53]
	v_mfma_f32_16x16x32_bf16 v[54:57], v[238:241], v[138:141], v[54:57]
	v_exp_f32_e32 v72, v72
	v_mfma_f32_16x16x32_bf16 v[58:61], v[242:245], v[130:133], v[58:61]
	v_mfma_f32_16x16x32_bf16 v[62:65], v[242:245], v[138:141], v[62:65]
	v_exp_f32_e32 v73, v73
	v_mfma_f32_16x16x32_bf16 v[252:255], v[194:197], v[138:141], v[252:255]
	ds_read_b64_tr_b16 v[230:231], v191 offset:41984
	ds_read_b64_tr_b16 v[232:233], v191 offset:46080
	ds_read_b64_tr_b16 v[234:235], v192 offset:41984
	ds_read_b64_tr_b16 v[236:237], v192 offset:46080
	s_waitcnt lgkmcnt(8)
; #define SBAR() __builtin_amdgcn_sched_barrier(0)
; __device__ __forceinline__ void qkt(f32x16& p0, f32x16& p1, const bf16_t* Ks, const bf16x8* qr, int r32, int hi) {
;   p0 = f32x16{}; p1 = f32x16{};
;   for (int d0 = 0; d0 < 8; ++d0) { int cb = (d0 * 16 + hi * 8) * 2;
;     bf16x8 b0 = *reinterpret_cast<const bf16x8*>((const char*)Ks + KSWZ(r32, cb));
;     bf16x8 b1 = *reinterpret_cast<const bf16x8*>((const char*)Ks + KSWZ(32 + r32, cb));
;     p0 = __builtin_amdgcn_mfma_f32_32x32x16_bf16(b0, qr[d0], p0, 0, 0, 0);
;     p1 = __builtin_amdgcn_mfma_f32_32x32x16_bf16(b1, qr[d0], p1, 0, 0, 0); }
; }
; template <int D0> __device__ __forceinline__ void pv_rd(s16x4 (&r)[8], int vb) {
;   r[0] = tr_read<v_rd_off(D0, 0, 0)>(vb); r[1] = tr_read<v_rd_off(D0, 0, 1)>(vb); r[2] = tr_read<v_rd_off(D0, 1, 0)>(vb); r[3] = tr_read<v_rd_off(D0, 1, 1)>(vb);
;   r[4] = tr_read<v_rd_off(D0, 2, 0)>(vb); r[5] = tr_read<v_rd_off(D0, 2, 1)>(vb); r[6] = tr_read<v_rd_off(D0, 3, 0)>(vb); r[7] = tr_read<v_rd_off(D0, 3, 1)>(vb);
; }
; __device__ __forceinline__ void pv_mm(f32x16& od, const s16x4 (&r)[8], bf16x8 pa0, bf16x8 pa1, bf16x8 pa2, bf16x8 pa3) {
;     ...
;   od = __builtin_amdgcn_mfma_f32_32x32x16_bf16(pa0, PK(r[0], r[1]), od, 0, 0, 0);
;   od = __builtin_amdgcn_mfma_f32_32x32x16_bf16(pa1, PK(r[2], r[3]), od, 0, 0, 0);
;   od = __builtin_amdgcn_mfma_f32_32x32x16_bf16(pa2, PK(r[4], r[5]), od, 0, 0, 0);
;   od = __builtin_amdgcn_mfma_f32_32x32x16_bf16(pa3, PK(r[6], r[7]), od, 0, 0, 0);
;     ...
; }
; __device__ __forceinline__ void pv_d0(f32x16* o, int vb, bf16x8 pa0, bf16x8 pa1, bf16x8 pa2, bf16x8 pa3) {
;   s16x4 ra[8], rb[8];
;   pv_rd<0>(ra, vb); pv_rd<1>(rb, vb);
;   asm volatile("s_waitcnt lgkmcnt(8)" ::: "memory"); SBAR(); pv_mm(o[0], ra, pa0, pa1, pa2, pa3); pv_rd<2>(ra, vb);
;   asm volatile("s_waitcnt lgkmcnt(8)" ::: "memory"); SBAR(); pv_mm(o[1], rb, pa0, pa1, pa2, pa3); pv_rd<3>(rb, vb);
;   asm volatile("s_waitcnt lgkmcnt(8)" ::: "memory"); SBAR(); pv_mm(o[2], ra, pa0, pa1, pa2, pa3);
;   asm volatile("s_waitcnt lgkmcnt(0)" ::: "memory"); SBAR(); pv_mm(o[3], rb, pa0, pa1, pa2, pa3);
; }
	v_mfma_f32_16x16x32_bf16 v[2:5], v[214:217], v[134:137], v[2:5]
	v_exp_f32_e32 v74, v74
	v_mfma_f32_16x16x32_bf16 v[6:9], v[214:217], v[142:145], v[6:9]
	v_cvt_pk_bf16_f32 v130, v66, v67
	v_mfma_f32_16x16x32_bf16 v[10:13], v[218:221], v[134:137], v[10:13]
	v_exp_f32_e32 v75, v75
	v_mfma_f32_16x16x32_bf16 v[14:17], v[218:221], v[142:145], v[14:17]
	v_cvt_pk_bf16_f32 v131, v68, v69
	ds_read_b64_tr_b16 v[238:239], v191 offset:42496
	ds_read_b64_tr_b16 v[240:241], v191 offset:46592
	ds_read_b64_tr_b16 v[242:243], v192 offset:42496
	ds_read_b64_tr_b16 v[244:245], v192 offset:46592
	s_waitcnt lgkmcnt(8)
	v_mfma_f32_16x16x32_bf16 v[18:21], v[222:225], v[134:137], v[18:21]
	v_exp_f32_e32 v76, v76
	v_mfma_f32_16x16x32_bf16 v[22:25], v[222:225], v[142:145], v[22:25]
	v_cvt_pk_bf16_f32 v132, v74, v75
	v_mfma_f32_16x16x32_bf16 v[26:29], v[226:229], v[134:137], v[26:29]
	v_exp_f32_e32 v77, v77
	v_mfma_f32_16x16x32_bf16 v[30:33], v[226:229], v[142:145], v[30:33]
	v_cvt_pk_bf16_f32 v133, v76, v77
	v_mfma_f32_16x16x32_bf16 v[246:249], v[194:197], v[134:137], v[246:249]
	s_waitcnt lgkmcnt(4)
	v_mfma_f32_16x16x32_bf16 v[34:37], v[230:233], v[134:137], v[34:37]
	v_exp_f32_e32 v78, v78
	v_mfma_f32_16x16x32_bf16 v[38:41], v[230:233], v[142:145], v[38:41]
	v_cvt_pk_bf16_f32 v138, v70, v71
	v_mfma_f32_16x16x32_bf16 v[42:45], v[234:237], v[134:137], v[42:45]
	v_exp_f32_e32 v79, v79
	v_mfma_f32_16x16x32_bf16 v[46:49], v[234:237], v[142:145], v[46:49]
	v_cvt_pk_bf16_f32 v139, v72, v73
	s_waitcnt lgkmcnt(0)
	v_mfma_f32_16x16x32_bf16 v[50:53], v[238:241], v[134:137], v[50:53]
	v_exp_f32_e32 v80, v80
	v_mfma_f32_16x16x32_bf16 v[54:57], v[238:241], v[142:145], v[54:57]
	v_cvt_pk_bf16_f32 v140, v78, v79
	v_mfma_f32_16x16x32_bf16 v[58:61], v[242:245], v[134:137], v[58:61]
	v_exp_f32_e32 v81, v81
	v_mfma_f32_16x16x32_bf16 v[62:65], v[242:245], v[142:145], v[62:65]
	v_cvt_pk_bf16_f32 v141, v80, v81
	v_mfma_f32_16x16x32_bf16 v[252:255], v[194:197], v[142:145], v[252:255]
	s_add_i32 s97, s97, 1
	ds_read_b128 v[146:149], v187 offset:32768
	ds_read_b128 v[150:153], v188 offset:32768
	ds_read_b128 v[154:157], v189 offset:32768
	ds_read_b128 v[158:161], v190 offset:32768
	ds_read_b128 v[198:201], v187 offset:36864
	ds_read_b128 v[202:205], v188 offset:36864
	ds_read_b128 v[206:209], v189 offset:36864
	ds_read_b128 v[210:213], v190 offset:36864
	s_waitcnt lgkmcnt(6)
	v_mfma_f32_16x16x32_bf16 v[66:69], v[146:149], v[98:101], 0
	v_exp_f32_e32 v82, v82
	v_mfma_f32_16x16x32_bf16 v[70:73], v[146:149], v[114:117], 0
	v_exp_f32_e32 v83, v83
	v_mfma_f32_16x16x32_bf16 v[66:69], v[150:153], v[102:105], v[66:69]
	v_exp_f32_e32 v84, v84
	v_mfma_f32_16x16x32_bf16 v[70:73], v[150:153], v[118:121], v[70:73]
	v_exp_f32_e32 v85, v85
	ds_read_b128 v[146:149], v187 offset:40960
	ds_read_b128 v[150:153], v188 offset:40960
	s_waitcnt lgkmcnt(6)
	v_mfma_f32_16x16x32_bf16 v[66:69], v[154:157], v[106:109], v[66:69]
	v_exp_f32_e32 v86, v86
	v_mfma_f32_16x16x32_bf16 v[70:73], v[154:157], v[122:125], v[70:73]
	v_exp_f32_e32 v87, v87
	v_mfma_f32_16x16x32_bf16 v[66:69], v[158:161], v[110:113], v[66:69]
	v_exp_f32_e32 v88, v88
	v_mfma_f32_16x16x32_bf16 v[70:73], v[158:161], v[126:129], v[70:73]
	v_exp_f32_e32 v89, v89
	ds_read_b128 v[154:157], v189 offset:40960
	ds_read_b128 v[158:161], v190 offset:40960
	s_waitcnt lgkmcnt(6)
	v_mfma_f32_16x16x32_bf16 v[74:77], v[198:201], v[98:101], 0
	v_exp_f32_e32 v90, v90
	v_mfma_f32_16x16x32_bf16 v[78:81], v[198:201], v[114:117], 0
	v_exp_f32_e32 v91, v91
	v_cvt_pk_bf16_f32 v134, v82, v83
	v_mfma_f32_16x16x32_bf16 v[74:77], v[202:205], v[102:105], v[74:77]
	v_exp_f32_e32 v92, v92
	v_cvt_pk_bf16_f32 v135, v84, v85
	v_mfma_f32_16x16x32_bf16 v[78:81], v[202:205], v[118:121], v[78:81]
	v_exp_f32_e32 v93, v93
	v_cvt_pk_bf16_f32 v142, v86, v87
	ds_read_b128 v[198:201], v187 offset:45056
	ds_read_b128 v[202:205], v188 offset:45056
	s_waitcnt lgkmcnt(6)
	v_mfma_f32_16x16x32_bf16 v[74:77], v[206:209], v[106:109], v[74:77]
	v_exp_f32_e32 v94, v94
	v_cvt_pk_bf16_f32 v143, v88, v89
	v_mfma_f32_16x16x32_bf16 v[78:81], v[206:209], v[122:125], v[78:81]
	v_exp_f32_e32 v95, v95
	v_mfma_f32_16x16x32_bf16 v[74:77], v[210:213], v[110:113], v[74:77]
	v_exp_f32_e32 v96, v96
	v_mfma_f32_16x16x32_bf16 v[78:81], v[210:213], v[126:129], v[78:81]
	v_exp_f32_e32 v97, v97
	ds_read_b128 v[206:209], v189 offset:45056
	ds_read_b128 v[210:213], v190 offset:45056
	s_waitcnt lgkmcnt(6)
	v_mfma_f32_16x16x32_bf16 v[82:85], v[146:149], v[98:101], 0
	v_mfma_f32_16x16x32_bf16 v[86:89], v[146:149], v[114:117], 0
	v_cvt_pk_bf16_f32 v136, v90, v91
	v_mfma_f32_16x16x32_bf16 v[82:85], v[150:153], v[102:105], v[82:85]
	v_cvt_pk_bf16_f32 v137, v92, v93
	v_mfma_f32_16x16x32_bf16 v[86:89], v[150:153], v[118:121], v[86:89]
	v_cvt_pk_bf16_f32 v144, v94, v95
	s_waitcnt lgkmcnt(4)
	v_mfma_f32_16x16x32_bf16 v[82:85], v[154:157], v[106:109], v[82:85]
	v_cvt_pk_bf16_f32 v145, v96, v97
	v_mfma_f32_16x16x32_bf16 v[86:89], v[154:157], v[122:125], v[86:89]
	v_mfma_f32_16x16x32_bf16 v[82:85], v[158:161], v[110:113], v[82:85]
	v_mfma_f32_16x16x32_bf16 v[86:89], v[158:161], v[126:129], v[86:89]
	s_waitcnt lgkmcnt(2)
	v_mfma_f32_16x16x32_bf16 v[90:93], v[198:201], v[98:101], 0
	v_mfma_f32_16x16x32_bf16 v[94:97], v[198:201], v[114:117], 0
	v_mfma_f32_16x16x32_bf16 v[90:93], v[202:205], v[102:105], v[90:93]
	v_mfma_f32_16x16x32_bf16 v[94:97], v[202:205], v[118:121], v[94:97]
	ds_read_b64_tr_b16 v[214:215], v180 offset:0
	ds_read_b64_tr_b16 v[216:217], v180 offset:4096
	ds_read_b64_tr_b16 v[218:219], v181 offset:0
	ds_read_b64_tr_b16 v[220:221], v181 offset:4096
	ds_read_b64_tr_b16 v[222:223], v180 offset:512
	ds_read_b64_tr_b16 v[224:225], v180 offset:4608
	ds_read_b64_tr_b16 v[226:227], v181 offset:512
	ds_read_b64_tr_b16 v[228:229], v181 offset:4608
	ds_read_b64_tr_b16 v[230:231], v180 offset:1024
	ds_read_b64_tr_b16 v[232:233], v180 offset:5120
	ds_read_b64_tr_b16 v[234:235], v181 offset:1024
	ds_read_b64_tr_b16 v[236:237], v181 offset:5120
	s_waitcnt lgkmcnt(12)
	v_mfma_f32_16x16x32_bf16 v[90:93], v[206:209], v[106:109], v[90:93]
	v_mfma_f32_16x16x32_bf16 v[94:97], v[206:209], v[122:125], v[94:97]
	v_mfma_f32_16x16x32_bf16 v[90:93], v[210:213], v[110:113], v[90:93]
	v_mfma_f32_16x16x32_bf16 v[94:97], v[210:213], v[126:129], v[94:97]
	s_waitcnt vmcnt(0) lgkmcnt(0)
	s_barrier
	s_cmp_ge_u32 s97, 130
	s_cbranch_scc1 .Lf16_se_N2
	s_add_i32 m0, s96, 0x8000
	s_nop 0
	global_load_lds_dwordx4 v170, s[2:3]
	s_add_i32 m0, s96, 0xa000
	s_nop 0
	global_load_lds_dwordx4 v172, s[2:3]
	s_add_i32 m0, s96, 0xc000
	s_nop 0
	global_load_lds_dwordx4 v171, s[2:3]
	s_add_i32 m0, s96, 0xe000
	s_nop 0
	global_load_lds_dwordx4 v173, s[2:3]
	s_add_u32 s2, s2, 0x4000
	s_addc_u32 s3, s3, 0
; #define SBAR() __builtin_amdgcn_sched_barrier(0)
; template <int D0> __device__ __forceinline__ void pv_rd(s16x4 (&r)[8], int vb) {
;   r[0] = tr_read<v_rd_off(D0, 0, 0)>(vb); r[1] = tr_read<v_rd_off(D0, 0, 1)>(vb); r[2] = tr_read<v_rd_off(D0, 1, 0)>(vb); r[3] = tr_read<v_rd_off(D0, 1, 1)>(vb);
;   r[4] = tr_read<v_rd_off(D0, 2, 0)>(vb); r[5] = tr_read<v_rd_off(D0, 2, 1)>(vb); r[6] = tr_read<v_rd_off(D0, 3, 0)>(vb); r[7] = tr_read<v_rd_off(D0, 3, 1)>(vb);
; }
; __device__ __forceinline__ void pv_mm(f32x16& od, const s16x4 (&r)[8], bf16x8 pa0, bf16x8 pa1, bf16x8 pa2, bf16x8 pa3) {
;     ...
;   od = __builtin_amdgcn_mfma_f32_32x32x16_bf16(pa0, PK(r[0], r[1]), od, 0, 0, 0);
;   od = __builtin_amdgcn_mfma_f32_32x32x16_bf16(pa1, PK(r[2], r[3]), od, 0, 0, 0);
;   od = __builtin_amdgcn_mfma_f32_32x32x16_bf16(pa2, PK(r[4], r[5]), od, 0, 0, 0);
;   od = __builtin_amdgcn_mfma_f32_32x32x16_bf16(pa3, PK(r[6], r[7]), od, 0, 0, 0);
;     ...
; }
; __device__ __forceinline__ void pv_d0(f32x16* o, int vb, bf16x8 pa0, bf16x8 pa1, bf16x8 pa2, bf16x8 pa3) {
;   s16x4 ra[8], rb[8];
;   pv_rd<0>(ra, vb); pv_rd<1>(rb, vb);
;   asm volatile("s_waitcnt lgkmcnt(8)" ::: "memory"); SBAR(); pv_mm(o[0], ra, pa0, pa1, pa2, pa3); pv_rd<2>(ra, vb);
;   asm volatile("s_waitcnt lgkmcnt(8)" ::: "memory"); SBAR(); pv_mm(o[1], rb, pa0, pa1, pa2, pa3); pv_rd<3>(rb, vb);
;   asm volatile("s_waitcnt lgkmcnt(8)" ::: "memory"); SBAR(); pv_mm(o[2], ra, pa0, pa1, pa2, pa3);
;   asm volatile("s_waitcnt lgkmcnt(0)" ::: "memory"); SBAR(); pv_mm(o[3], rb, pa0, pa1, pa2, pa3);
; }
.Lf16_se_N2:
	s_waitcnt lgkmcnt(8)
	v_mfma_f32_16x16x32_bf16 v[2:5], v[214:217], v[130:133], v[2:5]
	v_mfma_f32_16x16x32_bf16 v[6:9], v[214:217], v[138:141], v[6:9]
	v_exp_f32_e32 v66, v66
	v_mfma_f32_16x16x32_bf16 v[10:13], v[218:221], v[130:133], v[10:13]
	v_mfma_f32_16x16x32_bf16 v[14:17], v[218:221], v[138:141], v[14:17]
	v_exp_f32_e32 v67, v67
	ds_read_b64_tr_b16 v[238:239], v180 offset:1536
	ds_read_b64_tr_b16 v[240:241], v180 offset:5632
	ds_read_b64_tr_b16 v[242:243], v181 offset:1536
	ds_read_b64_tr_b16 v[244:245], v181 offset:5632
	s_waitcnt lgkmcnt(8)
	v_mfma_f32_16x16x32_bf16 v[18:21], v[222:225], v[130:133], v[18:21]
	v_mfma_f32_16x16x32_bf16 v[22:25], v[222:225], v[138:141], v[22:25]
	v_exp_f32_e32 v68, v68
	v_mfma_f32_16x16x32_bf16 v[26:29], v[226:229], v[130:133], v[26:29]
	v_mfma_f32_16x16x32_bf16 v[30:33], v[226:229], v[138:141], v[30:33]
	v_exp_f32_e32 v69, v69
	v_mfma_f32_16x16x32_bf16 v[246:249], v[194:197], v[130:133], v[246:249]
	ds_read_b64_tr_b16 v[214:215], v180 offset:8192
	ds_read_b64_tr_b16 v[216:217], v180 offset:12288
	ds_read_b64_tr_b16 v[218:219], v181 offset:8192
	ds_read_b64_tr_b16 v[220:221], v181 offset:12288
	s_waitcnt lgkmcnt(8)
	v_mfma_f32_16x16x32_bf16 v[34:37], v[230:233], v[130:133], v[34:37]
	v_mfma_f32_16x16x32_bf16 v[38:41], v[230:233], v[138:141], v[38:41]
	v_exp_f32_e32 v70, v70
	v_mfma_f32_16x16x32_bf16 v[42:45], v[234:237], v[130:133], v[42:45]
	v_mfma_f32_16x16x32_bf16 v[46:49], v[234:237], v[138:141], v[46:49]
	v_exp_f32_e32 v71, v71
	ds_read_b64_tr_b16 v[222:223], v180 offset:8704
	ds_read_b64_tr_b16 v[224:225], v180 offset:12800
	ds_read_b64_tr_b16 v[226:227], v181 offset:8704
	ds_read_b64_tr_b16 v[228:229], v181 offset:12800
	s_waitcnt lgkmcnt(8)
	v_mfma_f32_16x16x32_bf16 v[50:53], v[238:241], v[130:133], v[50:53]
	v_mfma_f32_16x16x32_bf16 v[54:57], v[238:241], v[138:141], v[54:57]
	v_exp_f32_e32 v72, v72
	v_mfma_f32_16x16x32_bf16 v[58:61], v[242:245], v[130:133], v[58:61]
	v_mfma_f32_16x16x32_bf16 v[62:65], v[242:245], v[138:141], v[62:65]
	v_exp_f32_e32 v73, v73
	v_mfma_f32_16x16x32_bf16 v[252:255], v[194:197], v[138:141], v[252:255]
	ds_read_b64_tr_b16 v[230:231], v180 offset:9216
	ds_read_b64_tr_b16 v[232:233], v180 offset:13312
	ds_read_b64_tr_b16 v[234:235], v181 offset:9216
	ds_read_b64_tr_b16 v[236:237], v181 offset:13312
	s_waitcnt lgkmcnt(8)
	v_mfma_f32_16x16x32_bf16 v[2:5], v[214:217], v[134:137], v[2:5]
	v_exp_f32_e32 v74, v74
	v_mfma_f32_16x16x32_bf16 v[6:9], v[214:217], v[142:145], v[6:9]
	v_cvt_pk_bf16_f32 v130, v66, v67
	v_mfma_f32_16x16x32_bf16 v[10:13], v[218:221], v[134:137], v[10:13]
	v_exp_f32_e32 v75, v75
	v_mfma_f32_16x16x32_bf16 v[14:17], v[218:221], v[142:145], v[14:17]
	v_cvt_pk_bf16_f32 v131, v68, v69
	ds_read_b64_tr_b16 v[238:239], v180 offset:9728
	ds_read_b64_tr_b16 v[240:241], v180 offset:13824
	ds_read_b64_tr_b16 v[242:243], v181 offset:9728
	ds_read_b64_tr_b16 v[244:245], v181 offset:13824
	s_waitcnt lgkmcnt(8)
	v_mfma_f32_16x16x32_bf16 v[18:21], v[222:225], v[134:137], v[18:21]
	v_exp_f32_e32 v76, v76
	v_mfma_f32_16x16x32_bf16 v[22:25], v[222:225], v[142:145], v[22:25]
	v_cvt_pk_bf16_f32 v132, v74, v75
	v_mfma_f32_16x16x32_bf16 v[26:29], v[226:229], v[134:137], v[26:29]
	v_exp_f32_e32 v77, v77
	v_mfma_f32_16x16x32_bf16 v[30:33], v[226:229], v[142:145], v[30:33]
	v_cvt_pk_bf16_f32 v133, v76, v77
	v_mfma_f32_16x16x32_bf16 v[246:249], v[194:197], v[134:137], v[246:249]
	s_waitcnt lgkmcnt(4)
	v_mfma_f32_16x16x32_bf16 v[34:37], v[230:233], v[134:137], v[34:37]
	v_exp_f32_e32 v78, v78
	v_mfma_f32_16x16x32_bf16 v[38:41], v[230:233], v[142:145], v[38:41]
	v_cvt_pk_bf16_f32 v138, v70, v71
	v_mfma_f32_16x16x32_bf16 v[42:45], v[234:237], v[134:137], v[42:45]
	v_exp_f32_e32 v79, v79
	v_mfma_f32_16x16x32_bf16 v[46:49], v[234:237], v[142:145], v[46:49]
	v_cvt_pk_bf16_f32 v139, v72, v73
	s_waitcnt lgkmcnt(0)
	v_mfma_f32_16x16x32_bf16 v[50:53], v[238:241], v[134:137], v[50:53]
	v_exp_f32_e32 v80, v80
	v_mfma_f32_16x16x32_bf16 v[54:57], v[238:241], v[142:145], v[54:57]
	v_cvt_pk_bf16_f32 v140, v78, v79
	v_mfma_f32_16x16x32_bf16 v[58:61], v[242:245], v[134:137], v[58:61]
	v_exp_f32_e32 v81, v81
	v_mfma_f32_16x16x32_bf16 v[62:65], v[242:245], v[142:145], v[62:65]
	v_cvt_pk_bf16_f32 v141, v80, v81
	v_mfma_f32_16x16x32_bf16 v[252:255], v[194:197], v[142:145], v[252:255]
	s_add_i32 s97, s97, 1
	s_cmp_lt_u32 s97, 132
	s_cbranch_scc0 .Lf16_done
; #define SBAR() __builtin_amdgcn_sched_barrier(0)
; #define ATT_SYNC(jn) do { ATT_WAIT_BAR(); if ((jn) < NT) ATT_DMA((jn), (jn) & 3); } while (0)
; __device__ __forceinline__ void qkt(f32x16& p0, f32x16& p1, const bf16_t* Ks, const bf16x8* qr, int r32, int hi) {
;   p0 = f32x16{}; p1 = f32x16{};
;   for (int d0 = 0; d0 < 8; ++d0) { int cb = (d0 * 16 + hi * 8) * 2;
;     bf16x8 b0 = *reinterpret_cast<const bf16x8*>((const char*)Ks + KSWZ(r32, cb));
;     bf16x8 b1 = *reinterpret_cast<const bf16x8*>((const char*)Ks + KSWZ(32 + r32, cb));
;     p0 = __builtin_amdgcn_mfma_f32_32x32x16_bf16(b0, qr[d0], p0, 0, 0, 0);
;     p1 = __builtin_amdgcn_mfma_f32_32x32x16_bf16(b1, qr[d0], p1, 0, 0, 0); }
; }
; __device__ __forceinline__ void attn_dma_body(const bf16_t* __restrict__ Qb, int ldq, int tpos0, const float* __restrict__ rope, const float* __restrict__ qgain, ...
;     ...
;   for (int j = 1; j + 1 < NT; j += 2) {
;     { SBAR(); qkt(pB0, pB1, (const bf16_t*)(lds + (j & 3) * SHM_SLOT), qr, r32, hi);
;       finishSM(pA0, pA1, alA, l_reg, pa0, pa1, pa2, pa3); s16x4 va[8]; pv_rd<0>(va, vb0 + ((j - 1) & 3) * (int)SHM_SLOT); SBAR();
;       if (!lead) ATT_SYNC(j + 2);
;       pv_d0_pre(o, vb0 + ((j - 1) & 3) * (int)SHM_SLOT, va, pa0, pa1, pa2, pa3); partialSM(pB0, pB1, m_reg, mnB, alB);
	ds_read_b128 v[146:149], v183 offset:0
	ds_read_b128 v[150:153], v184 offset:0
	ds_read_b128 v[154:157], v185 offset:0
	ds_read_b128 v[158:161], v186 offset:0
	ds_read_b128 v[198:201], v183 offset:4096
	ds_read_b128 v[202:205], v184 offset:4096
	ds_read_b128 v[206:209], v185 offset:4096
	ds_read_b128 v[210:213], v186 offset:4096
	s_waitcnt lgkmcnt(6)
	v_mfma_f32_16x16x32_bf16 v[66:69], v[146:149], v[98:101], 0
	v_exp_f32_e32 v82, v82
	v_mfma_f32_16x16x32_bf16 v[70:73], v[146:149], v[114:117], 0
	v_exp_f32_e32 v83, v83
	v_mfma_f32_16x16x32_bf16 v[66:69], v[150:153], v[102:105], v[66:69]
	v_exp_f32_e32 v84, v84
	v_mfma_f32_16x16x32_bf16 v[70:73], v[150:153], v[118:121], v[70:73]
	v_exp_f32_e32 v85, v85
	ds_read_b128 v[146:149], v183 offset:8192
	ds_read_b128 v[150:153], v184 offset:8192
	s_waitcnt lgkmcnt(6)
	v_mfma_f32_16x16x32_bf16 v[66:69], v[154:157], v[106:109], v[66:69]
	v_exp_f32_e32 v86, v86
	v_mfma_f32_16x16x32_bf16 v[70:73], v[154:157], v[122:125], v[70:73]
	v_exp_f32_e32 v87, v87
	v_mfma_f32_16x16x32_bf16 v[66:69], v[158:161], v[110:113], v[66:69]
	v_exp_f32_e32 v88, v88
	v_mfma_f32_16x16x32_bf16 v[70:73], v[158:161], v[126:129], v[70:73]
	v_exp_f32_e32 v89, v89
	ds_read_b128 v[154:157], v185 offset:8192
	ds_read_b128 v[158:161], v186 offset:8192
	s_waitcnt lgkmcnt(6)
	v_mfma_f32_16x16x32_bf16 v[74:77], v[198:201], v[98:101], 0
	v_exp_f32_e32 v90, v90
	v_mfma_f32_16x16x32_bf16 v[78:81], v[198:201], v[114:117], 0
	v_exp_f32_e32 v91, v91
	v_cvt_pk_bf16_f32 v134, v82, v83
	v_mfma_f32_16x16x32_bf16 v[74:77], v[202:205], v[102:105], v[74:77]
	v_exp_f32_e32 v92, v92
	v_cvt_pk_bf16_f32 v135, v84, v85
	v_mfma_f32_16x16x32_bf16 v[78:81], v[202:205], v[118:121], v[78:81]
	v_exp_f32_e32 v93, v93
	v_cvt_pk_bf16_f32 v142, v86, v87
	ds_read_b128 v[198:201], v183 offset:12288
	ds_read_b128 v[202:205], v184 offset:12288
	s_waitcnt lgkmcnt(6)
	v_mfma_f32_16x16x32_bf16 v[74:77], v[206:209], v[106:109], v[74:77]
	v_exp_f32_e32 v94, v94
	v_cvt_pk_bf16_f32 v143, v88, v89
	v_mfma_f32_16x16x32_bf16 v[78:81], v[206:209], v[122:125], v[78:81]
	v_exp_f32_e32 v95, v95
	v_mfma_f32_16x16x32_bf16 v[74:77], v[210:213], v[110:113], v[74:77]
	v_exp_f32_e32 v96, v96
	v_mfma_f32_16x16x32_bf16 v[78:81], v[210:213], v[126:129], v[78:81]
	v_exp_f32_e32 v97, v97
	ds_read_b128 v[206:209], v185 offset:12288
	ds_read_b128 v[210:213], v186 offset:12288
	s_waitcnt lgkmcnt(6)
	v_mfma_f32_16x16x32_bf16 v[82:85], v[146:149], v[98:101], 0
	v_mfma_f32_16x16x32_bf16 v[86:89], v[146:149], v[114:117], 0
	v_cvt_pk_bf16_f32 v136, v90, v91
	v_mfma_f32_16x16x32_bf16 v[82:85], v[150:153], v[102:105], v[82:85]
	v_cvt_pk_bf16_f32 v137, v92, v93
	v_mfma_f32_16x16x32_bf16 v[86:89], v[150:153], v[118:121], v[86:89]
	v_cvt_pk_bf16_f32 v144, v94, v95
	s_waitcnt lgkmcnt(4)
	v_mfma_f32_16x16x32_bf16 v[82:85], v[154:157], v[106:109], v[82:85]
	v_cvt_pk_bf16_f32 v145, v96, v97
	v_mfma_f32_16x16x32_bf16 v[86:89], v[154:157], v[122:125], v[86:89]
	v_mfma_f32_16x16x32_bf16 v[82:85], v[158:161], v[110:113], v[82:85]
	v_mfma_f32_16x16x32_bf16 v[86:89], v[158:161], v[126:129], v[86:89]
	s_waitcnt lgkmcnt(2)
	v_mfma_f32_16x16x32_bf16 v[90:93], v[198:201], v[98:101], 0
	v_mfma_f32_16x16x32_bf16 v[94:97], v[198:201], v[114:117], 0
	v_mfma_f32_16x16x32_bf16 v[90:93], v[202:205], v[102:105], v[90:93]
	v_mfma_f32_16x16x32_bf16 v[94:97], v[202:205], v[118:121], v[94:97]
	ds_read_b64_tr_b16 v[214:215], v180 offset:32768
	ds_read_b64_tr_b16 v[216:217], v180 offset:36864
	ds_read_b64_tr_b16 v[218:219], v181 offset:32768
	ds_read_b64_tr_b16 v[220:221], v181 offset:36864
	ds_read_b64_tr_b16 v[222:223], v180 offset:33280
	ds_read_b64_tr_b16 v[224:225], v180 offset:37376
	ds_read_b64_tr_b16 v[226:227], v181 offset:33280
	ds_read_b64_tr_b16 v[228:229], v181 offset:37376
	ds_read_b64_tr_b16 v[230:231], v180 offset:33792
	ds_read_b64_tr_b16 v[232:233], v180 offset:37888
	ds_read_b64_tr_b16 v[234:235], v181 offset:33792
	ds_read_b64_tr_b16 v[236:237], v181 offset:37888
	s_waitcnt lgkmcnt(12)
	v_mfma_f32_16x16x32_bf16 v[90:93], v[206:209], v[106:109], v[90:93]
	v_mfma_f32_16x16x32_bf16 v[94:97], v[206:209], v[122:125], v[94:97]
	v_mfma_f32_16x16x32_bf16 v[90:93], v[210:213], v[110:113], v[90:93]
	v_mfma_f32_16x16x32_bf16 v[94:97], v[210:213], v[126:129], v[94:97]
	s_waitcnt vmcnt(0) lgkmcnt(0)
	s_barrier
	s_cmp_ge_u32 s97, 130
	s_cbranch_scc1 .Lf16_se_N3
	s_add_i32 m0, s96, 0x10000
	s_nop 0
	global_load_lds_dwordx4 v170, s[2:3]
	s_add_i32 m0, s96, 0x12000
	s_nop 0
	global_load_lds_dwordx4 v172, s[2:3]
	s_add_i32 m0, s96, 0x14000
	s_nop 0
	global_load_lds_dwordx4 v171, s[2:3]
	s_add_i32 m0, s96, 0x16000
	s_nop 0
	global_load_lds_dwordx4 v173, s[2:3]
	s_add_u32 s2, s2, 0x4000
	s_addc_u32 s3, s3, 0
; #define SBAR() __builtin_amdgcn_sched_barrier(0)
; template <int D0> __device__ __forceinline__ void pv_rd(s16x4 (&r)[8], int vb) {
;   r[0] = tr_read<v_rd_off(D0, 0, 0)>(vb); r[1] = tr_read<v_rd_off(D0, 0, 1)>(vb); r[2] = tr_read<v_rd_off(D0, 1, 0)>(vb); r[3] = tr_read<v_rd_off(D0, 1, 1)>(vb);
;   r[4] = tr_read<v_rd_off(D0, 2, 0)>(vb); r[5] = tr_read<v_rd_off(D0, 2, 1)>(vb); r[6] = tr_read<v_rd_off(D0, 3, 0)>(vb); r[7] = tr_read<v_rd_off(D0, 3, 1)>(vb);
; }
; __device__ __forceinline__ void pv_mm(f32x16& od, const s16x4 (&r)[8], bf16x8 pa0, bf16x8 pa1, bf16x8 pa2, bf16x8 pa3) {
;     ...
;   od = __builtin_amdgcn_mfma_f32_32x32x16_bf16(pa0, PK(r[0], r[1]), od, 0, 0, 0);
;   od = __builtin_amdgcn_mfma_f32_32x32x16_bf16(pa1, PK(r[2], r[3]), od, 0, 0, 0);
;   od = __builtin_amdgcn_mfma_f32_32x32x16_bf16(pa2, PK(r[4], r[5]), od, 0, 0, 0);
;   od = __builtin_amdgcn_mfma_f32_32x32x16_bf16(pa3, PK(r[6], r[7]), od, 0, 0, 0);
;     ...
; }
; __device__ __forceinline__ void pv_d0(f32x16* o, int vb, bf16x8 pa0, bf16x8 pa1, bf16x8 pa2, bf16x8 pa3) {
;   s16x4 ra[8], rb[8];
;   pv_rd<0>(ra, vb); pv_rd<1>(rb, vb);
;   asm volatile("s_waitcnt lgkmcnt(8)" ::: "memory"); SBAR(); pv_mm(o[0], ra, pa0, pa1, pa2, pa3); pv_rd<2>(ra, vb);
;   asm volatile("s_waitcnt lgkmcnt(8)" ::: "memory"); SBAR(); pv_mm(o[1], rb, pa0, pa1, pa2, pa3); pv_rd<3>(rb, vb);
;   asm volatile("s_waitcnt lgkmcnt(8)" ::: "memory"); SBAR(); pv_mm(o[2], ra, pa0, pa1, pa2, pa3);
;   asm volatile("s_waitcnt lgkmcnt(0)" ::: "memory"); SBAR(); pv_mm(o[3], rb, pa0, pa1, pa2, pa3);
; }
.Lf16_se_N3:
	s_waitcnt lgkmcnt(8)
	v_mfma_f32_16x16x32_bf16 v[2:5], v[214:217], v[130:133], v[2:5]
	v_mfma_f32_16x16x32_bf16 v[6:9], v[214:217], v[138:141], v[6:9]
	v_exp_f32_e32 v66, v66
	v_mfma_f32_16x16x32_bf16 v[10:13], v[218:221], v[130:133], v[10:13]
	v_mfma_f32_16x16x32_bf16 v[14:17], v[218:221], v[138:141], v[14:17]
	v_exp_f32_e32 v67, v67
	ds_read_b64_tr_b16 v[238:239], v180 offset:34304
	ds_read_b64_tr_b16 v[240:241], v180 offset:38400
	ds_read_b64_tr_b16 v[242:243], v181 offset:34304
	ds_read_b64_tr_b16 v[244:245], v181 offset:38400
	s_waitcnt lgkmcnt(8)
	v_mfma_f32_16x16x32_bf16 v[18:21], v[222:225], v[130:133], v[18:21]
	v_mfma_f32_16x16x32_bf16 v[22:25], v[222:225], v[138:141], v[22:25]
	v_exp_f32_e32 v68, v68
	v_mfma_f32_16x16x32_bf16 v[26:29], v[226:229], v[130:133], v[26:29]
	v_mfma_f32_16x16x32_bf16 v[30:33], v[226:229], v[138:141], v[30:33]
	v_exp_f32_e32 v69, v69
	v_mfma_f32_16x16x32_bf16 v[246:249], v[194:197], v[130:133], v[246:249]
	ds_read_b64_tr_b16 v[214:215], v180 offset:40960
	ds_read_b64_tr_b16 v[216:217], v180 offset:45056
	ds_read_b64_tr_b16 v[218:219], v181 offset:40960
	ds_read_b64_tr_b16 v[220:221], v181 offset:45056
	s_waitcnt lgkmcnt(8)
	v_mfma_f32_16x16x32_bf16 v[34:37], v[230:233], v[130:133], v[34:37]
	v_mfma_f32_16x16x32_bf16 v[38:41], v[230:233], v[138:141], v[38:41]
	v_exp_f32_e32 v70, v70
	v_mfma_f32_16x16x32_bf16 v[42:45], v[234:237], v[130:133], v[42:45]
	v_mfma_f32_16x16x32_bf16 v[46:49], v[234:237], v[138:141], v[46:49]
	v_exp_f32_e32 v71, v71
	ds_read_b64_tr_b16 v[222:223], v180 offset:41472
	ds_read_b64_tr_b16 v[224:225], v180 offset:45568
	ds_read_b64_tr_b16 v[226:227], v181 offset:41472
	ds_read_b64_tr_b16 v[228:229], v181 offset:45568
	s_waitcnt lgkmcnt(8)
	v_mfma_f32_16x16x32_bf16 v[50:53], v[238:241], v[130:133], v[50:53]
	v_mfma_f32_16x16x32_bf16 v[54:57], v[238:241], v[138:141], v[54:57]
	v_exp_f32_e32 v72, v72
	v_mfma_f32_16x16x32_bf16 v[58:61], v[242:245], v[130:133], v[58:61]
	v_mfma_f32_16x16x32_bf16 v[62:65], v[242:245], v[138:141], v[62:65]
	v_exp_f32_e32 v73, v73
	v_mfma_f32_16x16x32_bf16 v[252:255], v[194:197], v[138:141], v[252:255]
	ds_read_b64_tr_b16 v[230:231], v180 offset:41984
	ds_read_b64_tr_b16 v[232:233], v180 offset:46080
	ds_read_b64_tr_b16 v[234:235], v181 offset:41984
	ds_read_b64_tr_b16 v[236:237], v181 offset:46080
	s_waitcnt lgkmcnt(8)
	v_mfma_f32_16x16x32_bf16 v[2:5], v[214:217], v[134:137], v[2:5]
	v_exp_f32_e32 v74, v74
	v_mfma_f32_16x16x32_bf16 v[6:9], v[214:217], v[142:145], v[6:9]
	v_cvt_pk_bf16_f32 v130, v66, v67
	v_mfma_f32_16x16x32_bf16 v[10:13], v[218:221], v[134:137], v[10:13]
	v_exp_f32_e32 v75, v75
	v_mfma_f32_16x16x32_bf16 v[14:17], v[218:221], v[142:145], v[14:17]
	v_cvt_pk_bf16_f32 v131, v68, v69
	ds_read_b64_tr_b16 v[238:239], v180 offset:42496
	ds_read_b64_tr_b16 v[240:241], v180 offset:46592
	ds_read_b64_tr_b16 v[242:243], v181 offset:42496
	ds_read_b64_tr_b16 v[244:245], v181 offset:46592
	s_waitcnt lgkmcnt(8)
	v_mfma_f32_16x16x32_bf16 v[18:21], v[222:225], v[134:137], v[18:21]
	v_exp_f32_e32 v76, v76
	v_mfma_f32_16x16x32_bf16 v[22:25], v[222:225], v[142:145], v[22:25]
	v_cvt_pk_bf16_f32 v132, v74, v75
	v_mfma_f32_16x16x32_bf16 v[26:29], v[226:229], v[134:137], v[26:29]
	v_exp_f32_e32 v77, v77
	v_mfma_f32_16x16x32_bf16 v[30:33], v[226:229], v[142:145], v[30:33]
	v_cvt_pk_bf16_f32 v133, v76, v77
	v_mfma_f32_16x16x32_bf16 v[246:249], v[194:197], v[134:137], v[246:249]
	s_waitcnt lgkmcnt(4)
	v_mfma_f32_16x16x32_bf16 v[34:37], v[230:233], v[134:137], v[34:37]
	v_exp_f32_e32 v78, v78
	v_mfma_f32_16x16x32_bf16 v[38:41], v[230:233], v[142:145], v[38:41]
	v_cvt_pk_bf16_f32 v138, v70, v71
	v_mfma_f32_16x16x32_bf16 v[42:45], v[234:237], v[134:137], v[42:45]
	v_exp_f32_e32 v79, v79
	v_mfma_f32_16x16x32_bf16 v[46:49], v[234:237], v[142:145], v[46:49]
	v_cvt_pk_bf16_f32 v139, v72, v73
	s_waitcnt lgkmcnt(0)
	v_mfma_f32_16x16x32_bf16 v[50:53], v[238:241], v[134:137], v[50:53]
	v_exp_f32_e32 v80, v80
	v_mfma_f32_16x16x32_bf16 v[54:57], v[238:241], v[142:145], v[54:57]
	v_cvt_pk_bf16_f32 v140, v78, v79
	v_mfma_f32_16x16x32_bf16 v[58:61], v[242:245], v[134:137], v[58:61]
	v_exp_f32_e32 v81, v81
	v_mfma_f32_16x16x32_bf16 v[62:65], v[242:245], v[142:145], v[62:65]
	v_cvt_pk_bf16_f32 v141, v80, v81
	v_mfma_f32_16x16x32_bf16 v[252:255], v[194:197], v[142:145], v[252:255]
	s_add_i32 s97, s97, 1
	s_branch .Lf16_N_loop
	.p2align 6
; #define SBAR() __builtin_amdgcn_sched_barrier(0)
; #define RESC(a) do { if (__any((a) < 1.f)) { if (hi == 0) al_l[r32] = (a); asm volatile("s_waitcnt lgkmcnt(0)" ::: "memory"); \
;     for (int d = 0; d < 4; ++d) for (int r = 0; r < 16; ++r) o[d][r] *= al_l[crow(r, hi)]; } } while (0)
; #define RESC(a) do { if (__any((a) < 1.f)) { if (hi == 0) al_l[r32] = (a); asm volatile("s_waitcnt lgkmcnt(0)" ::: "memory"); \
;     for (int d = 0; d < 4; ++d) for (int r = 0; r < 16; ++r) o[d][r] *= al_l[crow(r, hi)]; } } while (0)
; #define ATT_SYNC(jn) do { ATT_WAIT_BAR(); if ((jn) < NT) ATT_DMA((jn), (jn) & 3); } while (0)
; __device__ __forceinline__ void attn_dma_body(const bf16_t* __restrict__ Qb, int ldq, int tpos0, const float* __restrict__ rope, const float* __restrict__ qgain, ...
;     ...
;   for (int j = 1; j + 1 < NT; j += 2) {
;     { SBAR(); qkt(pB0, pB1, (const bf16_t*)(lds + (j & 3) * SHM_SLOT), qr, r32, hi);
;       finishSM(pA0, pA1, alA, l_reg, pa0, pa1, pa2, pa3); s16x4 va[8]; pv_rd<0>(va, vb0 + ((j - 1) & 3) * (int)SHM_SLOT); SBAR();
;       if (!lead) ATT_SYNC(j + 2);
;       pv_d0_pre(o, vb0 + ((j - 1) & 3) * (int)SHM_SLOT, va, pa0, pa1, pa2, pa3); partialSM(pB0, pB1, m_reg, mnB, alB);
;       if (lead) ATT_SYNC(j + 2);
;       RESC(alB); }
;     { SBAR(); qkt(pA0, pA1, (const bf16_t*)(lds + ((j + 1) & 3) * SHM_SLOT), qr, r32, hi);
;       finishSM(pB0, pB1, alB, l_reg, pa0, pa1, pa2, pa3); s16x4 va[8]; pv_rd<0>(va, vb0 + (j & 3) * (int)SHM_SLOT); SBAR();
;       if (!lead) ATT_SYNC(j + 3);
;       pv_d0_pre(o, vb0 + (j & 3) * (int)SHM_SLOT, va, pa0, pa1, pa2, pa3); partialSM(pA0, pA1, m_reg, mnA, alA);
;       if (lead) ATT_SYNC(j + 3);
;       RESC(alA); }
;   }
.Lf16_L_loop:
	ds_read_b128 v[146:149], v183 offset:32768
	ds_read_b128 v[150:153], v184 offset:32768
	ds_read_b128 v[154:157], v185 offset:32768
	ds_read_b128 v[158:161], v186 offset:32768
	ds_read_b128 v[198:201], v183 offset:36864
	ds_read_b128 v[202:205], v184 offset:36864
	ds_read_b128 v[206:209], v185 offset:36864
	ds_read_b128 v[210:213], v186 offset:36864
	s_waitcnt lgkmcnt(6)
	v_mfma_f32_16x16x32_bf16 v[66:69], v[146:149], v[98:101], 0
	v_exp_f32_e32 v82, v82
	v_mfma_f32_16x16x32_bf16 v[70:73], v[146:149], v[114:117], 0
	v_exp_f32_e32 v83, v83
	v_mfma_f32_16x16x32_bf16 v[66:69], v[150:153], v[102:105], v[66:69]
	v_exp_f32_e32 v84, v84
	v_mfma_f32_16x16x32_bf16 v[70:73], v[150:153], v[118:121], v[70:73]
	v_exp_f32_e32 v85, v85
	ds_read_b128 v[146:149], v183 offset:40960
	ds_read_b128 v[150:153], v184 offset:40960
	s_waitcnt lgkmcnt(6)
	v_mfma_f32_16x16x32_bf16 v[66:69], v[154:157], v[106:109], v[66:69]
	v_exp_f32_e32 v86, v86
	v_mfma_f32_16x16x32_bf16 v[70:73], v[154:157], v[122:125], v[70:73]
	v_exp_f32_e32 v87, v87
	v_mfma_f32_16x16x32_bf16 v[66:69], v[158:161], v[110:113], v[66:69]
	v_exp_f32_e32 v88, v88
	v_mfma_f32_16x16x32_bf16 v[70:73], v[158:161], v[126:129], v[70:73]
	v_exp_f32_e32 v89, v89
	ds_read_b128 v[154:157], v185 offset:40960
	ds_read_b128 v[158:161], v186 offset:40960
	s_waitcnt lgkmcnt(6)
	v_mfma_f32_16x16x32_bf16 v[74:77], v[198:201], v[98:101], 0
	v_exp_f32_e32 v90, v90
	v_mfma_f32_16x16x32_bf16 v[78:81], v[198:201], v[114:117], 0
	v_exp_f32_e32 v91, v91
	v_cvt_pk_bf16_f32 v134, v82, v83
	v_mfma_f32_16x16x32_bf16 v[74:77], v[202:205], v[102:105], v[74:77]
	v_exp_f32_e32 v92, v92
	v_cvt_pk_bf16_f32 v135, v84, v85
	v_mfma_f32_16x16x32_bf16 v[78:81], v[202:205], v[118:121], v[78:81]
	v_exp_f32_e32 v93, v93
	v_cvt_pk_bf16_f32 v142, v86, v87
	ds_read_b128 v[198:201], v183 offset:45056
	ds_read_b128 v[202:205], v184 offset:45056
	s_waitcnt lgkmcnt(6)
	v_mfma_f32_16x16x32_bf16 v[74:77], v[206:209], v[106:109], v[74:77]
	v_exp_f32_e32 v94, v94
	v_cvt_pk_bf16_f32 v143, v88, v89
	v_mfma_f32_16x16x32_bf16 v[78:81], v[206:209], v[122:125], v[78:81]
	v_exp_f32_e32 v95, v95
	v_mfma_f32_16x16x32_bf16 v[74:77], v[210:213], v[110:113], v[74:77]
	v_exp_f32_e32 v96, v96
	v_mfma_f32_16x16x32_bf16 v[78:81], v[210:213], v[126:129], v[78:81]
	v_exp_f32_e32 v97, v97
	ds_read_b128 v[206:209], v185 offset:45056
	ds_read_b128 v[210:213], v186 offset:45056
	s_waitcnt lgkmcnt(6)
	v_mfma_f32_16x16x32_bf16 v[82:85], v[146:149], v[98:101], 0
	v_mfma_f32_16x16x32_bf16 v[86:89], v[146:149], v[114:117], 0
	v_cvt_pk_bf16_f32 v136, v90, v91
	v_mfma_f32_16x16x32_bf16 v[82:85], v[150:153], v[102:105], v[82:85]
	v_cvt_pk_bf16_f32 v137, v92, v93
	v_mfma_f32_16x16x32_bf16 v[86:89], v[150:153], v[118:121], v[86:89]
	v_cvt_pk_bf16_f32 v144, v94, v95
	s_waitcnt lgkmcnt(4)
	v_mfma_f32_16x16x32_bf16 v[82:85], v[154:157], v[106:109], v[82:85]
	v_cvt_pk_bf16_f32 v145, v96, v97
	v_mfma_f32_16x16x32_bf16 v[86:89], v[154:157], v[122:125], v[86:89]
	v_mfma_f32_16x16x32_bf16 v[82:85], v[158:161], v[110:113], v[82:85]
	v_mfma_f32_16x16x32_bf16 v[86:89], v[158:161], v[126:129], v[86:89]
	s_waitcnt lgkmcnt(2)
	v_mfma_f32_16x16x32_bf16 v[90:93], v[198:201], v[98:101], 0
	v_mfma_f32_16x16x32_bf16 v[94:97], v[198:201], v[114:117], 0
	v_mfma_f32_16x16x32_bf16 v[90:93], v[202:205], v[102:105], v[90:93]
	v_mfma_f32_16x16x32_bf16 v[94:97], v[202:205], v[118:121], v[94:97]
	ds_read_b64_tr_b16 v[214:215], v191 offset:0
	ds_read_b64_tr_b16 v[216:217], v191 offset:4096
	ds_read_b64_tr_b16 v[218:219], v192 offset:0
	ds_read_b64_tr_b16 v[220:221], v192 offset:4096
	ds_read_b64_tr_b16 v[222:223], v191 offset:512
	ds_read_b64_tr_b16 v[224:225], v191 offset:4608
	ds_read_b64_tr_b16 v[226:227], v192 offset:512
	ds_read_b64_tr_b16 v[228:229], v192 offset:4608
	ds_read_b64_tr_b16 v[230:231], v191 offset:1024
	ds_read_b64_tr_b16 v[232:233], v191 offset:5120
	ds_read_b64_tr_b16 v[234:235], v192 offset:1024
	ds_read_b64_tr_b16 v[236:237], v192 offset:5120
	s_waitcnt lgkmcnt(12)
	v_mfma_f32_16x16x32_bf16 v[90:93], v[206:209], v[106:109], v[90:93]
	v_mfma_f32_16x16x32_bf16 v[94:97], v[206:209], v[122:125], v[94:97]
	v_mfma_f32_16x16x32_bf16 v[90:93], v[210:213], v[110:113], v[90:93]
	v_mfma_f32_16x16x32_bf16 v[94:97], v[210:213], v[126:129], v[94:97]
	s_waitcnt lgkmcnt(8)
	v_mfma_f32_16x16x32_bf16 v[2:5], v[214:217], v[130:133], v[2:5]
	v_mfma_f32_16x16x32_bf16 v[6:9], v[214:217], v[138:141], v[6:9]
	v_exp_f32_e32 v66, v66
	v_mfma_f32_16x16x32_bf16 v[10:13], v[218:221], v[130:133], v[10:13]
	v_mfma_f32_16x16x32_bf16 v[14:17], v[218:221], v[138:141], v[14:17]
	v_exp_f32_e32 v67, v67
	ds_read_b64_tr_b16 v[238:239], v191 offset:1536
	ds_read_b64_tr_b16 v[240:241], v191 offset:5632
	ds_read_b64_tr_b16 v[242:243], v192 offset:1536
	ds_read_b64_tr_b16 v[244:245], v192 offset:5632
	s_waitcnt lgkmcnt(8)
	v_mfma_f32_16x16x32_bf16 v[18:21], v[222:225], v[130:133], v[18:21]
	v_mfma_f32_16x16x32_bf16 v[22:25], v[222:225], v[138:141], v[22:25]
	v_exp_f32_e32 v68, v68
	v_mfma_f32_16x16x32_bf16 v[26:29], v[226:229], v[130:133], v[26:29]
	v_mfma_f32_16x16x32_bf16 v[30:33], v[226:229], v[138:141], v[30:33]
	v_exp_f32_e32 v69, v69
	v_mfma_f32_16x16x32_bf16 v[246:249], v[194:197], v[130:133], v[246:249]
	ds_read_b64_tr_b16 v[214:215], v191 offset:8192
	ds_read_b64_tr_b16 v[216:217], v191 offset:12288
	ds_read_b64_tr_b16 v[218:219], v192 offset:8192
	ds_read_b64_tr_b16 v[220:221], v192 offset:12288
	s_waitcnt lgkmcnt(8)
; #define SBAR() __builtin_amdgcn_sched_barrier(0)
; #define RESC(a) do { if (__any((a) < 1.f)) { if (hi == 0) al_l[r32] = (a); asm volatile("s_waitcnt lgkmcnt(0)" ::: "memory"); \
;     for (int d = 0; d < 4; ++d) for (int r = 0; r < 16; ++r) o[d][r] *= al_l[crow(r, hi)]; } } while (0)
; #define RESC(a) do { if (__any((a) < 1.f)) { if (hi == 0) al_l[r32] = (a); asm volatile("s_waitcnt lgkmcnt(0)" ::: "memory"); \
;     for (int d = 0; d < 4; ++d) for (int r = 0; r < 16; ++r) o[d][r] *= al_l[crow(r, hi)]; } } while (0)
; #define ATT_SYNC(jn) do { ATT_WAIT_BAR(); if ((jn) < NT) ATT_DMA((jn), (jn) & 3); } while (0)
; __device__ __forceinline__ void attn_dma_body(const bf16_t* __restrict__ Qb, int ldq, int tpos0, const float* __restrict__ rope, const float* __restrict__ qgain, ...
;     ...
;   for (int j = 1; j + 1 < NT; j += 2) {
;     { SBAR(); qkt(pB0, pB1, (const bf16_t*)(lds + (j & 3) * SHM_SLOT), qr, r32, hi);
;       finishSM(pA0, pA1, alA, l_reg, pa0, pa1, pa2, pa3); s16x4 va[8]; pv_rd<0>(va, vb0 + ((j - 1) & 3) * (int)SHM_SLOT); SBAR();
;       if (!lead) ATT_SYNC(j + 2);
;       pv_d0_pre(o, vb0 + ((j - 1) & 3) * (int)SHM_SLOT, va, pa0, pa1, pa2, pa3); partialSM(pB0, pB1, m_reg, mnB, alB);
;       if (lead) ATT_SYNC(j + 2);
;       RESC(alB); }
;     { SBAR(); qkt(pA0, pA1, (const bf16_t*)(lds + ((j + 1) & 3) * SHM_SLOT), qr, r32, hi);
;       finishSM(pB0, pB1, alB, l_reg, pa0, pa1, pa2, pa3); s16x4 va[8]; pv_rd<0>(va, vb0 + (j & 3) * (int)SHM_SLOT); SBAR();
;       if (!lead) ATT_SYNC(j + 3);
;       pv_d0_pre(o, vb0 + (j & 3) * (int)SHM_SLOT, va, pa0, pa1, pa2, pa3); partialSM(pA0, pA1, m_reg, mnA, alA);
;       if (lead) ATT_SYNC(j + 3);
;       RESC(alA); }
;   }
	v_mfma_f32_16x16x32_bf16 v[34:37], v[230:233], v[130:133], v[34:37]
	v_mfma_f32_16x16x32_bf16 v[38:41], v[230:233], v[138:141], v[38:41]
	v_exp_f32_e32 v70, v70
	v_mfma_f32_16x16x32_bf16 v[42:45], v[234:237], v[130:133], v[42:45]
	v_mfma_f32_16x16x32_bf16 v[46:49], v[234:237], v[138:141], v[46:49]
	v_exp_f32_e32 v71, v71
	ds_read_b64_tr_b16 v[222:223], v191 offset:8704
	ds_read_b64_tr_b16 v[224:225], v191 offset:12800
	ds_read_b64_tr_b16 v[226:227], v192 offset:8704
	ds_read_b64_tr_b16 v[228:229], v192 offset:12800
	s_waitcnt lgkmcnt(8)
	v_mfma_f32_16x16x32_bf16 v[50:53], v[238:241], v[130:133], v[50:53]
	v_mfma_f32_16x16x32_bf16 v[54:57], v[238:241], v[138:141], v[54:57]
	v_exp_f32_e32 v72, v72
	v_mfma_f32_16x16x32_bf16 v[58:61], v[242:245], v[130:133], v[58:61]
	v_mfma_f32_16x16x32_bf16 v[62:65], v[242:245], v[138:141], v[62:65]
	v_exp_f32_e32 v73, v73
	v_mfma_f32_16x16x32_bf16 v[252:255], v[194:197], v[138:141], v[252:255]
	ds_read_b64_tr_b16 v[230:231], v191 offset:9216
	ds_read_b64_tr_b16 v[232:233], v191 offset:13312
	ds_read_b64_tr_b16 v[234:235], v192 offset:9216
	ds_read_b64_tr_b16 v[236:237], v192 offset:13312
	s_waitcnt lgkmcnt(8)
	v_mfma_f32_16x16x32_bf16 v[2:5], v[214:217], v[134:137], v[2:5]
	v_exp_f32_e32 v74, v74
	v_mfma_f32_16x16x32_bf16 v[6:9], v[214:217], v[142:145], v[6:9]
	v_cvt_pk_bf16_f32 v130, v66, v67
	v_mfma_f32_16x16x32_bf16 v[10:13], v[218:221], v[134:137], v[10:13]
	v_exp_f32_e32 v75, v75
	v_mfma_f32_16x16x32_bf16 v[14:17], v[218:221], v[142:145], v[14:17]
	v_cvt_pk_bf16_f32 v131, v68, v69
	ds_read_b64_tr_b16 v[238:239], v191 offset:9728
	ds_read_b64_tr_b16 v[240:241], v191 offset:13824
	ds_read_b64_tr_b16 v[242:243], v192 offset:9728
	ds_read_b64_tr_b16 v[244:245], v192 offset:13824
	s_waitcnt lgkmcnt(8)
	v_mfma_f32_16x16x32_bf16 v[18:21], v[222:225], v[134:137], v[18:21]
	v_exp_f32_e32 v76, v76
	v_mfma_f32_16x16x32_bf16 v[22:25], v[222:225], v[142:145], v[22:25]
	v_cvt_pk_bf16_f32 v132, v74, v75
	v_mfma_f32_16x16x32_bf16 v[26:29], v[226:229], v[134:137], v[26:29]
	v_exp_f32_e32 v77, v77
	v_mfma_f32_16x16x32_bf16 v[30:33], v[226:229], v[142:145], v[30:33]
	v_cvt_pk_bf16_f32 v133, v76, v77
	v_mfma_f32_16x16x32_bf16 v[246:249], v[194:197], v[134:137], v[246:249]
	s_waitcnt lgkmcnt(4)
	v_mfma_f32_16x16x32_bf16 v[34:37], v[230:233], v[134:137], v[34:37]
	v_exp_f32_e32 v78, v78
	v_mfma_f32_16x16x32_bf16 v[38:41], v[230:233], v[142:145], v[38:41]
	v_cvt_pk_bf16_f32 v138, v70, v71
	v_mfma_f32_16x16x32_bf16 v[42:45], v[234:237], v[134:137], v[42:45]
	v_exp_f32_e32 v79, v79
	v_mfma_f32_16x16x32_bf16 v[46:49], v[234:237], v[142:145], v[46:49]
	v_cvt_pk_bf16_f32 v139, v72, v73
	s_waitcnt lgkmcnt(0)
	v_mfma_f32_16x16x32_bf16 v[50:53], v[238:241], v[134:137], v[50:53]
	v_exp_f32_e32 v80, v80
	v_mfma_f32_16x16x32_bf16 v[54:57], v[238:241], v[142:145], v[54:57]
	v_cvt_pk_bf16_f32 v140, v78, v79
	v_mfma_f32_16x16x32_bf16 v[58:61], v[242:245], v[134:137], v[58:61]
	v_exp_f32_e32 v81, v81
	v_mfma_f32_16x16x32_bf16 v[62:65], v[242:245], v[142:145], v[62:65]
	v_cvt_pk_bf16_f32 v141, v80, v81
	v_mfma_f32_16x16x32_bf16 v[252:255], v[194:197], v[142:145], v[252:255]
	s_waitcnt vmcnt(0) lgkmcnt(0)
	s_barrier
	s_cmp_ge_u32 s97, 130
	s_cbranch_scc1 .Lf16_se_L0
	s_add_i32 m0, s96, 0x18000
	s_nop 0
	global_load_lds_dwordx4 v170, s[2:3]
	s_add_i32 m0, s96, 0x1a000
	s_nop 0
	global_load_lds_dwordx4 v172, s[2:3]
	s_add_i32 m0, s96, 0x1c000
	s_nop 0
	global_load_lds_dwordx4 v171, s[2:3]
	s_add_i32 m0, s96, 0x1e000
	s_nop 0
	global_load_lds_dwordx4 v173, s[2:3]
	s_add_u32 s2, s2, 0x4000
	s_addc_u32 s3, s3, 0
.Lf16_se_L0:
	s_add_i32 s97, s97, 1
	ds_read_b128 v[146:149], v187 offset:0
	ds_read_b128 v[150:153], v188 offset:0
	ds_read_b128 v[154:157], v189 offset:0
	ds_read_b128 v[158:161], v190 offset:0
	ds_read_b128 v[198:201], v187 offset:4096
	ds_read_b128 v[202:205], v188 offset:4096
	ds_read_b128 v[206:209], v189 offset:4096
	ds_read_b128 v[210:213], v190 offset:4096
	s_waitcnt lgkmcnt(6)
	v_mfma_f32_16x16x32_bf16 v[66:69], v[146:149], v[98:101], 0
	v_exp_f32_e32 v82, v82
	v_mfma_f32_16x16x32_bf16 v[70:73], v[146:149], v[114:117], 0
	v_exp_f32_e32 v83, v83
	v_mfma_f32_16x16x32_bf16 v[66:69], v[150:153], v[102:105], v[66:69]
	v_exp_f32_e32 v84, v84
	v_mfma_f32_16x16x32_bf16 v[70:73], v[150:153], v[118:121], v[70:73]
	v_exp_f32_e32 v85, v85
	ds_read_b128 v[146:149], v187 offset:8192
	ds_read_b128 v[150:153], v188 offset:8192
	s_waitcnt lgkmcnt(6)
	v_mfma_f32_16x16x32_bf16 v[66:69], v[154:157], v[106:109], v[66:69]
	v_exp_f32_e32 v86, v86
	v_mfma_f32_16x16x32_bf16 v[70:73], v[154:157], v[122:125], v[70:73]
	v_exp_f32_e32 v87, v87
	v_mfma_f32_16x16x32_bf16 v[66:69], v[158:161], v[110:113], v[66:69]
	v_exp_f32_e32 v88, v88
	v_mfma_f32_16x16x32_bf16 v[70:73], v[158:161], v[126:129], v[70:73]
	v_exp_f32_e32 v89, v89
	ds_read_b128 v[154:157], v189 offset:8192
	ds_read_b128 v[158:161], v190 offset:8192
	s_waitcnt lgkmcnt(6)
	v_mfma_f32_16x16x32_bf16 v[74:77], v[198:201], v[98:101], 0
	v_exp_f32_e32 v90, v90
	v_mfma_f32_16x16x32_bf16 v[78:81], v[198:201], v[114:117], 0
	v_exp_f32_e32 v91, v91
	v_cvt_pk_bf16_f32 v134, v82, v83
	v_mfma_f32_16x16x32_bf16 v[74:77], v[202:205], v[102:105], v[74:77]
	v_exp_f32_e32 v92, v92
	v_cvt_pk_bf16_f32 v135, v84, v85
	v_mfma_f32_16x16x32_bf16 v[78:81], v[202:205], v[118:121], v[78:81]
	v_exp_f32_e32 v93, v93
	v_cvt_pk_bf16_f32 v142, v86, v87
	ds_read_b128 v[198:201], v187 offset:12288
	ds_read_b128 v[202:205], v188 offset:12288
	s_waitcnt lgkmcnt(6)
; #define SBAR() __builtin_amdgcn_sched_barrier(0)
; #define RESC(a) do { if (__any((a) < 1.f)) { if (hi == 0) al_l[r32] = (a); asm volatile("s_waitcnt lgkmcnt(0)" ::: "memory"); \
;     for (int d = 0; d < 4; ++d) for (int r = 0; r < 16; ++r) o[d][r] *= al_l[crow(r, hi)]; } } while (0)
; #define RESC(a) do { if (__any((a) < 1.f)) { if (hi == 0) al_l[r32] = (a); asm volatile("s_waitcnt lgkmcnt(0)" ::: "memory"); \
;     for (int d = 0; d < 4; ++d) for (int r = 0; r < 16; ++r) o[d][r] *= al_l[crow(r, hi)]; } } while (0)
; #define ATT_SYNC(jn) do { ATT_WAIT_BAR(); if ((jn) < NT) ATT_DMA((jn), (jn) & 3); } while (0)
; __device__ __forceinline__ void attn_dma_body(const bf16_t* __restrict__ Qb, int ldq, int tpos0, const float* __restrict__ rope, const float* __restrict__ qgain, ...
;     ...
;   for (int j = 1; j + 1 < NT; j += 2) {
;     { SBAR(); qkt(pB0, pB1, (const bf16_t*)(lds + (j & 3) * SHM_SLOT), qr, r32, hi);
;       finishSM(pA0, pA1, alA, l_reg, pa0, pa1, pa2, pa3); s16x4 va[8]; pv_rd<0>(va, vb0 + ((j - 1) & 3) * (int)SHM_SLOT); SBAR();
;       if (!lead) ATT_SYNC(j + 2);
;       pv_d0_pre(o, vb0 + ((j - 1) & 3) * (int)SHM_SLOT, va, pa0, pa1, pa2, pa3); partialSM(pB0, pB1, m_reg, mnB, alB);
;       if (lead) ATT_SYNC(j + 2);
;       RESC(alB); }
;     { SBAR(); qkt(pA0, pA1, (const bf16_t*)(lds + ((j + 1) & 3) * SHM_SLOT), qr, r32, hi);
;       finishSM(pB0, pB1, alB, l_reg, pa0, pa1, pa2, pa3); s16x4 va[8]; pv_rd<0>(va, vb0 + (j & 3) * (int)SHM_SLOT); SBAR();
;       if (!lead) ATT_SYNC(j + 3);
;       pv_d0_pre(o, vb0 + (j & 3) * (int)SHM_SLOT, va, pa0, pa1, pa2, pa3); partialSM(pA0, pA1, m_reg, mnA, alA);
;       if (lead) ATT_SYNC(j + 3);
;       RESC(alA); }
;   }
	v_mfma_f32_16x16x32_bf16 v[74:77], v[206:209], v[106:109], v[74:77]
	v_exp_f32_e32 v94, v94
	v_cvt_pk_bf16_f32 v143, v88, v89
	v_mfma_f32_16x16x32_bf16 v[78:81], v[206:209], v[122:125], v[78:81]
	v_exp_f32_e32 v95, v95
	v_mfma_f32_16x16x32_bf16 v[74:77], v[210:213], v[110:113], v[74:77]
	v_exp_f32_e32 v96, v96
	v_mfma_f32_16x16x32_bf16 v[78:81], v[210:213], v[126:129], v[78:81]
	v_exp_f32_e32 v97, v97
	ds_read_b128 v[206:209], v189 offset:12288
	ds_read_b128 v[210:213], v190 offset:12288
	s_waitcnt lgkmcnt(6)
	v_mfma_f32_16x16x32_bf16 v[82:85], v[146:149], v[98:101], 0
	v_mfma_f32_16x16x32_bf16 v[86:89], v[146:149], v[114:117], 0
	v_cvt_pk_bf16_f32 v136, v90, v91
	v_mfma_f32_16x16x32_bf16 v[82:85], v[150:153], v[102:105], v[82:85]
	v_cvt_pk_bf16_f32 v137, v92, v93
	v_mfma_f32_16x16x32_bf16 v[86:89], v[150:153], v[118:121], v[86:89]
	v_cvt_pk_bf16_f32 v144, v94, v95
	s_waitcnt lgkmcnt(4)
	v_mfma_f32_16x16x32_bf16 v[82:85], v[154:157], v[106:109], v[82:85]
	v_cvt_pk_bf16_f32 v145, v96, v97
	v_mfma_f32_16x16x32_bf16 v[86:89], v[154:157], v[122:125], v[86:89]
	v_mfma_f32_16x16x32_bf16 v[82:85], v[158:161], v[110:113], v[82:85]
	v_mfma_f32_16x16x32_bf16 v[86:89], v[158:161], v[126:129], v[86:89]
	s_waitcnt lgkmcnt(2)
	v_mfma_f32_16x16x32_bf16 v[90:93], v[198:201], v[98:101], 0
	v_mfma_f32_16x16x32_bf16 v[94:97], v[198:201], v[114:117], 0
	v_mfma_f32_16x16x32_bf16 v[90:93], v[202:205], v[102:105], v[90:93]
	v_mfma_f32_16x16x32_bf16 v[94:97], v[202:205], v[118:121], v[94:97]
	ds_read_b64_tr_b16 v[214:215], v191 offset:32768
	ds_read_b64_tr_b16 v[216:217], v191 offset:36864
	ds_read_b64_tr_b16 v[218:219], v192 offset:32768
	ds_read_b64_tr_b16 v[220:221], v192 offset:36864
	ds_read_b64_tr_b16 v[222:223], v191 offset:33280
	ds_read_b64_tr_b16 v[224:225], v191 offset:37376
	ds_read_b64_tr_b16 v[226:227], v192 offset:33280
	ds_read_b64_tr_b16 v[228:229], v192 offset:37376
	ds_read_b64_tr_b16 v[230:231], v191 offset:33792
	ds_read_b64_tr_b16 v[232:233], v191 offset:37888
	ds_read_b64_tr_b16 v[234:235], v192 offset:33792
	ds_read_b64_tr_b16 v[236:237], v192 offset:37888
	s_waitcnt lgkmcnt(12)
	v_mfma_f32_16x16x32_bf16 v[90:93], v[206:209], v[106:109], v[90:93]
	v_mfma_f32_16x16x32_bf16 v[94:97], v[206:209], v[122:125], v[94:97]
	v_mfma_f32_16x16x32_bf16 v[90:93], v[210:213], v[110:113], v[90:93]
	v_mfma_f32_16x16x32_bf16 v[94:97], v[210:213], v[126:129], v[94:97]
	s_waitcnt lgkmcnt(8)
	v_mfma_f32_16x16x32_bf16 v[2:5], v[214:217], v[130:133], v[2:5]
	v_mfma_f32_16x16x32_bf16 v[6:9], v[214:217], v[138:141], v[6:9]
	v_exp_f32_e32 v66, v66
	v_mfma_f32_16x16x32_bf16 v[10:13], v[218:221], v[130:133], v[10:13]
	v_mfma_f32_16x16x32_bf16 v[14:17], v[218:221], v[138:141], v[14:17]
	v_exp_f32_e32 v67, v67
	ds_read_b64_tr_b16 v[238:239], v191 offset:34304
	ds_read_b64_tr_b16 v[240:241], v191 offset:38400
	ds_read_b64_tr_b16 v[242:243], v192 offset:34304
	ds_read_b64_tr_b16 v[244:245], v192 offset:38400
	s_waitcnt lgkmcnt(8)
	v_mfma_f32_16x16x32_bf16 v[18:21], v[222:225], v[130:133], v[18:21]
	v_mfma_f32_16x16x32_bf16 v[22:25], v[222:225], v[138:141], v[22:25]
	v_exp_f32_e32 v68, v68
	v_mfma_f32_16x16x32_bf16 v[26:29], v[226:229], v[130:133], v[26:29]
	v_mfma_f32_16x16x32_bf16 v[30:33], v[226:229], v[138:141], v[30:33]
	v_exp_f32_e32 v69, v69
	v_mfma_f32_16x16x32_bf16 v[246:249], v[194:197], v[130:133], v[246:249]
	ds_read_b64_tr_b16 v[214:215], v191 offset:40960
	ds_read_b64_tr_b16 v[216:217], v191 offset:45056
	ds_read_b64_tr_b16 v[218:219], v192 offset:40960
	ds_read_b64_tr_b16 v[220:221], v192 offset:45056
	s_waitcnt lgkmcnt(8)
	v_mfma_f32_16x16x32_bf16 v[34:37], v[230:233], v[130:133], v[34:37]
	v_mfma_f32_16x16x32_bf16 v[38:41], v[230:233], v[138:141], v[38:41]
	v_exp_f32_e32 v70, v70
	v_mfma_f32_16x16x32_bf16 v[42:45], v[234:237], v[130:133], v[42:45]
	v_mfma_f32_16x16x32_bf16 v[46:49], v[234:237], v[138:141], v[46:49]
	v_exp_f32_e32 v71, v71
	ds_read_b64_tr_b16 v[222:223], v191 offset:41472
	ds_read_b64_tr_b16 v[224:225], v191 offset:45568
	ds_read_b64_tr_b16 v[226:227], v192 offset:41472
	ds_read_b64_tr_b16 v[228:229], v192 offset:45568
	s_waitcnt lgkmcnt(8)
	v_mfma_f32_16x16x32_bf16 v[50:53], v[238:241], v[130:133], v[50:53]
	v_mfma_f32_16x16x32_bf16 v[54:57], v[238:241], v[138:141], v[54:57]
	v_exp_f32_e32 v72, v72
	v_mfma_f32_16x16x32_bf16 v[58:61], v[242:245], v[130:133], v[58:61]
	v_mfma_f32_16x16x32_bf16 v[62:65], v[242:245], v[138:141], v[62:65]
	v_exp_f32_e32 v73, v73
	v_mfma_f32_16x16x32_bf16 v[252:255], v[194:197], v[138:141], v[252:255]
	ds_read_b64_tr_b16 v[230:231], v191 offset:41984
	ds_read_b64_tr_b16 v[232:233], v191 offset:46080
	ds_read_b64_tr_b16 v[234:235], v192 offset:41984
	ds_read_b64_tr_b16 v[236:237], v192 offset:46080
	s_waitcnt lgkmcnt(8)
	v_mfma_f32_16x16x32_bf16 v[2:5], v[214:217], v[134:137], v[2:5]
	v_exp_f32_e32 v74, v74
	v_mfma_f32_16x16x32_bf16 v[6:9], v[214:217], v[142:145], v[6:9]
	v_cvt_pk_bf16_f32 v130, v66, v67
	v_mfma_f32_16x16x32_bf16 v[10:13], v[218:221], v[134:137], v[10:13]
	v_exp_f32_e32 v75, v75
	v_mfma_f32_16x16x32_bf16 v[14:17], v[218:221], v[142:145], v[14:17]
	v_cvt_pk_bf16_f32 v131, v68, v69
	ds_read_b64_tr_b16 v[238:239], v191 offset:42496
	ds_read_b64_tr_b16 v[240:241], v191 offset:46592
	ds_read_b64_tr_b16 v[242:243], v192 offset:42496
	ds_read_b64_tr_b16 v[244:245], v192 offset:46592
	s_waitcnt lgkmcnt(8)
	v_mfma_f32_16x16x32_bf16 v[18:21], v[222:225], v[134:137], v[18:21]
	v_exp_f32_e32 v76, v76
	v_mfma_f32_16x16x32_bf16 v[22:25], v[222:225], v[142:145], v[22:25]
	v_cvt_pk_bf16_f32 v132, v74, v75
	v_mfma_f32_16x16x32_bf16 v[26:29], v[226:229], v[134:137], v[26:29]
	v_exp_f32_e32 v77, v77
	v_mfma_f32_16x16x32_bf16 v[30:33], v[226:229], v[142:145], v[30:33]
	v_cvt_pk_bf16_f32 v133, v76, v77
	v_mfma_f32_16x16x32_bf16 v[246:249], v[194:197], v[134:137], v[246:249]
	s_waitcnt lgkmcnt(4)
	v_mfma_f32_16x16x32_bf16 v[34:37], v[230:233], v[134:137], v[34:37]
	v_exp_f32_e32 v78, v78
	v_mfma_f32_16x16x32_bf16 v[38:41], v[230:233], v[142:145], v[38:41]
	v_cvt_pk_bf16_f32 v138, v70, v71
	v_mfma_f32_16x16x32_bf16 v[42:45], v[234:237], v[134:137], v[42:45]
	v_exp_f32_e32 v79, v79
	v_mfma_f32_16x16x32_bf16 v[46:49], v[234:237], v[142:145], v[46:49]
	v_cvt_pk_bf16_f32 v139, v72, v73
	s_waitcnt lgkmcnt(0)
	v_mfma_f32_16x16x32_bf16 v[50:53], v[238:241], v[134:137], v[50:53]
	v_exp_f32_e32 v80, v80
	v_mfma_f32_16x16x32_bf16 v[54:57], v[238:241], v[142:145], v[54:57]
	v_cvt_pk_bf16_f32 v140, v78, v79
	v_mfma_f32_16x16x32_bf16 v[58:61], v[242:245], v[134:137], v[58:61]
	v_exp_f32_e32 v81, v81
	v_mfma_f32_16x16x32_bf16 v[62:65], v[242:245], v[142:145], v[62:65]
	v_cvt_pk_bf16_f32 v141, v80, v81
	v_mfma_f32_16x16x32_bf16 v[252:255], v[194:197], v[142:145], v[252:255]
	s_waitcnt vmcnt(0) lgkmcnt(0)
	s_barrier
; #define SBAR() __builtin_amdgcn_sched_barrier(0)
; #define RESC(a) do { if (__any((a) < 1.f)) { if (hi == 0) al_l[r32] = (a); asm volatile("s_waitcnt lgkmcnt(0)" ::: "memory"); \
;     for (int d = 0; d < 4; ++d) for (int r = 0; r < 16; ++r) o[d][r] *= al_l[crow(r, hi)]; } } while (0)
; #define RESC(a) do { if (__any((a) < 1.f)) { if (hi == 0) al_l[r32] = (a); asm volatile("s_waitcnt lgkmcnt(0)" ::: "memory"); \
;     for (int d = 0; d < 4; ++d) for (int r = 0; r < 16; ++r) o[d][r] *= al_l[crow(r, hi)]; } } while (0)
; #define ATT_SYNC(jn) do { ATT_WAIT_BAR(); if ((jn) < NT) ATT_DMA((jn), (jn) & 3); } while (0)
; __device__ __forceinline__ void attn_dma_body(const bf16_t* __restrict__ Qb, int ldq, int tpos0, const float* __restrict__ rope, const float* __restrict__ qgain, ...
;     ...
;   for (int j = 1; j + 1 < NT; j += 2) {
;     { SBAR(); qkt(pB0, pB1, (const bf16_t*)(lds + (j & 3) * SHM_SLOT), qr, r32, hi);
;       finishSM(pA0, pA1, alA, l_reg, pa0, pa1, pa2, pa3); s16x4 va[8]; pv_rd<0>(va, vb0 + ((j - 1) & 3) * (int)SHM_SLOT); SBAR();
;       if (!lead) ATT_SYNC(j + 2);
;       pv_d0_pre(o, vb0 + ((j - 1) & 3) * (int)SHM_SLOT, va, pa0, pa1, pa2, pa3); partialSM(pB0, pB1, m_reg, mnB, alB);
;       if (lead) ATT_SYNC(j + 2);
;       RESC(alB); }
;     { SBAR(); qkt(pA0, pA1, (const bf16_t*)(lds + ((j + 1) & 3) * SHM_SLOT), qr, r32, hi);
;       finishSM(pB0, pB1, alB, l_reg, pa0, pa1, pa2, pa3); s16x4 va[8]; pv_rd<0>(va, vb0 + (j & 3) * (int)SHM_SLOT); SBAR();
;       if (!lead) ATT_SYNC(j + 3);
;       pv_d0_pre(o, vb0 + (j & 3) * (int)SHM_SLOT, va, pa0, pa1, pa2, pa3); partialSM(pA0, pA1, m_reg, mnA, alA);
;       if (lead) ATT_SYNC(j + 3);
;       RESC(alA); }
;   }
	s_cmp_ge_u32 s97, 130
	s_cbranch_scc1 .Lf16_se_L1
	s_add_i32 m0, s96, 0x0
	s_nop 0
	global_load_lds_dwordx4 v170, s[2:3]
	s_add_i32 m0, s96, 0x2000
	s_nop 0
	global_load_lds_dwordx4 v172, s[2:3]
	s_add_i32 m0, s96, 0x4000
	s_nop 0
	global_load_lds_dwordx4 v171, s[2:3]
	s_add_i32 m0, s96, 0x6000
	s_nop 0
	global_load_lds_dwordx4 v173, s[2:3]
	s_add_u32 s2, s2, 0x4000
	s_addc_u32 s3, s3, 0
.Lf16_se_L1:
	s_add_i32 s97, s97, 1
	ds_read_b128 v[146:149], v187 offset:32768
	ds_read_b128 v[150:153], v188 offset:32768
	ds_read_b128 v[154:157], v189 offset:32768
	ds_read_b128 v[158:161], v190 offset:32768
	ds_read_b128 v[198:201], v187 offset:36864
	ds_read_b128 v[202:205], v188 offset:36864
	ds_read_b128 v[206:209], v189 offset:36864
	ds_read_b128 v[210:213], v190 offset:36864
	s_waitcnt lgkmcnt(6)
	v_mfma_f32_16x16x32_bf16 v[66:69], v[146:149], v[98:101], 0
	v_exp_f32_e32 v82, v82
	v_mfma_f32_16x16x32_bf16 v[70:73], v[146:149], v[114:117], 0
	v_exp_f32_e32 v83, v83
	v_mfma_f32_16x16x32_bf16 v[66:69], v[150:153], v[102:105], v[66:69]
	v_exp_f32_e32 v84, v84
	v_mfma_f32_16x16x32_bf16 v[70:73], v[150:153], v[118:121], v[70:73]
	v_exp_f32_e32 v85, v85
	ds_read_b128 v[146:149], v187 offset:40960
	ds_read_b128 v[150:153], v188 offset:40960
	s_waitcnt lgkmcnt(6)
	v_mfma_f32_16x16x32_bf16 v[66:69], v[154:157], v[106:109], v[66:69]
	v_exp_f32_e32 v86, v86
	v_mfma_f32_16x16x32_bf16 v[70:73], v[154:157], v[122:125], v[70:73]
	v_exp_f32_e32 v87, v87
	v_mfma_f32_16x16x32_bf16 v[66:69], v[158:161], v[110:113], v[66:69]
	v_exp_f32_e32 v88, v88
	v_mfma_f32_16x16x32_bf16 v[70:73], v[158:161], v[126:129], v[70:73]
	v_exp_f32_e32 v89, v89
	ds_read_b128 v[154:157], v189 offset:40960
	ds_read_b128 v[158:161], v190 offset:40960
	s_waitcnt lgkmcnt(6)
	v_mfma_f32_16x16x32_bf16 v[74:77], v[198:201], v[98:101], 0
	v_exp_f32_e32 v90, v90
	v_mfma_f32_16x16x32_bf16 v[78:81], v[198:201], v[114:117], 0
	v_exp_f32_e32 v91, v91
	v_cvt_pk_bf16_f32 v134, v82, v83
	v_mfma_f32_16x16x32_bf16 v[74:77], v[202:205], v[102:105], v[74:77]
	v_exp_f32_e32 v92, v92
	v_cvt_pk_bf16_f32 v135, v84, v85
	v_mfma_f32_16x16x32_bf16 v[78:81], v[202:205], v[118:121], v[78:81]
	v_exp_f32_e32 v93, v93
	v_cvt_pk_bf16_f32 v142, v86, v87
	ds_read_b128 v[198:201], v187 offset:45056
	ds_read_b128 v[202:205], v188 offset:45056
	s_waitcnt lgkmcnt(6)
	v_mfma_f32_16x16x32_bf16 v[74:77], v[206:209], v[106:109], v[74:77]
	v_exp_f32_e32 v94, v94
	v_cvt_pk_bf16_f32 v143, v88, v89
	v_mfma_f32_16x16x32_bf16 v[78:81], v[206:209], v[122:125], v[78:81]
	v_exp_f32_e32 v95, v95
	v_mfma_f32_16x16x32_bf16 v[74:77], v[210:213], v[110:113], v[74:77]
	v_exp_f32_e32 v96, v96
	v_mfma_f32_16x16x32_bf16 v[78:81], v[210:213], v[126:129], v[78:81]
	v_exp_f32_e32 v97, v97
	ds_read_b128 v[206:209], v189 offset:45056
	ds_read_b128 v[210:213], v190 offset:45056
	s_waitcnt lgkmcnt(6)
	v_mfma_f32_16x16x32_bf16 v[82:85], v[146:149], v[98:101], 0
	v_mfma_f32_16x16x32_bf16 v[86:89], v[146:149], v[114:117], 0
	v_cvt_pk_bf16_f32 v136, v90, v91
	v_mfma_f32_16x16x32_bf16 v[82:85], v[150:153], v[102:105], v[82:85]
	v_cvt_pk_bf16_f32 v137, v92, v93
	v_mfma_f32_16x16x32_bf16 v[86:89], v[150:153], v[118:121], v[86:89]
	v_cvt_pk_bf16_f32 v144, v94, v95
	s_waitcnt lgkmcnt(4)
	v_mfma_f32_16x16x32_bf16 v[82:85], v[154:157], v[106:109], v[82:85]
	v_cvt_pk_bf16_f32 v145, v96, v97
	v_mfma_f32_16x16x32_bf16 v[86:89], v[154:157], v[122:125], v[86:89]
	v_mfma_f32_16x16x32_bf16 v[82:85], v[158:161], v[110:113], v[82:85]
	v_mfma_f32_16x16x32_bf16 v[86:89], v[158:161], v[126:129], v[86:89]
	s_waitcnt lgkmcnt(2)
	v_mfma_f32_16x16x32_bf16 v[90:93], v[198:201], v[98:101], 0
	v_mfma_f32_16x16x32_bf16 v[94:97], v[198:201], v[114:117], 0
	v_mfma_f32_16x16x32_bf16 v[90:93], v[202:205], v[102:105], v[90:93]
	v_mfma_f32_16x16x32_bf16 v[94:97], v[202:205], v[118:121], v[94:97]
	ds_read_b64_tr_b16 v[214:215], v180 offset:0
	ds_read_b64_tr_b16 v[216:217], v180 offset:4096
	ds_read_b64_tr_b16 v[218:219], v181 offset:0
	ds_read_b64_tr_b16 v[220:221], v181 offset:4096
	ds_read_b64_tr_b16 v[222:223], v180 offset:512
	ds_read_b64_tr_b16 v[224:225], v180 offset:4608
	ds_read_b64_tr_b16 v[226:227], v181 offset:512
	ds_read_b64_tr_b16 v[228:229], v181 offset:4608
	ds_read_b64_tr_b16 v[230:231], v180 offset:1024
	ds_read_b64_tr_b16 v[232:233], v180 offset:5120
	ds_read_b64_tr_b16 v[234:235], v181 offset:1024
	ds_read_b64_tr_b16 v[236:237], v181 offset:5120
	s_waitcnt lgkmcnt(12)
	v_mfma_f32_16x16x32_bf16 v[90:93], v[206:209], v[106:109], v[90:93]
	v_mfma_f32_16x16x32_bf16 v[94:97], v[206:209], v[122:125], v[94:97]
	v_mfma_f32_16x16x32_bf16 v[90:93], v[210:213], v[110:113], v[90:93]
	v_mfma_f32_16x16x32_bf16 v[94:97], v[210:213], v[126:129], v[94:97]
	s_waitcnt lgkmcnt(8)
	v_mfma_f32_16x16x32_bf16 v[2:5], v[214:217], v[130:133], v[2:5]
	v_mfma_f32_16x16x32_bf16 v[6:9], v[214:217], v[138:141], v[6:9]
	v_exp_f32_e32 v66, v66
	v_mfma_f32_16x16x32_bf16 v[10:13], v[218:221], v[130:133], v[10:13]
	v_mfma_f32_16x16x32_bf16 v[14:17], v[218:221], v[138:141], v[14:17]
	v_exp_f32_e32 v67, v67
	ds_read_b64_tr_b16 v[238:239], v180 offset:1536
	ds_read_b64_tr_b16 v[240:241], v180 offset:5632
	ds_read_b64_tr_b16 v[242:243], v181 offset:1536
	ds_read_b64_tr_b16 v[244:245], v181 offset:5632
	s_waitcnt lgkmcnt(8)
	v_mfma_f32_16x16x32_bf16 v[18:21], v[222:225], v[130:133], v[18:21]
	v_mfma_f32_16x16x32_bf16 v[22:25], v[222:225], v[138:141], v[22:25]
	v_exp_f32_e32 v68, v68
	v_mfma_f32_16x16x32_bf16 v[26:29], v[226:229], v[130:133], v[26:29]
	v_mfma_f32_16x16x32_bf16 v[30:33], v[226:229], v[138:141], v[30:33]
	v_exp_f32_e32 v69, v69
	v_mfma_f32_16x16x32_bf16 v[246:249], v[194:197], v[130:133], v[246:249]
	ds_read_b64_tr_b16 v[214:215], v180 offset:8192
	ds_read_b64_tr_b16 v[216:217], v180 offset:12288
	ds_read_b64_tr_b16 v[218:219], v181 offset:8192
	ds_read_b64_tr_b16 v[220:221], v181 offset:12288
	s_waitcnt lgkmcnt(8)
; #define SBAR() __builtin_amdgcn_sched_barrier(0)
; #define RESC(a) do { if (__any((a) < 1.f)) { if (hi == 0) al_l[r32] = (a); asm volatile("s_waitcnt lgkmcnt(0)" ::: "memory"); \
;     for (int d = 0; d < 4; ++d) for (int r = 0; r < 16; ++r) o[d][r] *= al_l[crow(r, hi)]; } } while (0)
; #define RESC(a) do { if (__any((a) < 1.f)) { if (hi == 0) al_l[r32] = (a); asm volatile("s_waitcnt lgkmcnt(0)" ::: "memory"); \
;     for (int d = 0; d < 4; ++d) for (int r = 0; r < 16; ++r) o[d][r] *= al_l[crow(r, hi)]; } } while (0)
; #define ATT_SYNC(jn) do { ATT_WAIT_BAR(); if ((jn) < NT) ATT_DMA((jn), (jn) & 3); } while (0)
; __device__ __forceinline__ void attn_dma_body(const bf16_t* __restrict__ Qb, int ldq, int tpos0, const float* __restrict__ rope, const float* __restrict__ qgain, ...
;     ...
;   for (int j = 1; j + 1 < NT; j += 2) {
;     { SBAR(); qkt(pB0, pB1, (const bf16_t*)(lds + (j & 3) * SHM_SLOT), qr, r32, hi);
;       finishSM(pA0, pA1, alA, l_reg, pa0, pa1, pa2, pa3); s16x4 va[8]; pv_rd<0>(va, vb0 + ((j - 1) & 3) * (int)SHM_SLOT); SBAR();
;       if (!lead) ATT_SYNC(j + 2);
;       pv_d0_pre(o, vb0 + ((j - 1) & 3) * (int)SHM_SLOT, va, pa0, pa1, pa2, pa3); partialSM(pB0, pB1, m_reg, mnB, alB);
;       if (lead) ATT_SYNC(j + 2);
;       RESC(alB); }
;     { SBAR(); qkt(pA0, pA1, (const bf16_t*)(lds + ((j + 1) & 3) * SHM_SLOT), qr, r32, hi);
;       finishSM(pB0, pB1, alB, l_reg, pa0, pa1, pa2, pa3); s16x4 va[8]; pv_rd<0>(va, vb0 + (j & 3) * (int)SHM_SLOT); SBAR();
;       if (!lead) ATT_SYNC(j + 3);
;       pv_d0_pre(o, vb0 + (j & 3) * (int)SHM_SLOT, va, pa0, pa1, pa2, pa3); partialSM(pA0, pA1, m_reg, mnA, alA);
;       if (lead) ATT_SYNC(j + 3);
;       RESC(alA); }
;   }
	v_mfma_f32_16x16x32_bf16 v[34:37], v[230:233], v[130:133], v[34:37]
	v_mfma_f32_16x16x32_bf16 v[38:41], v[230:233], v[138:141], v[38:41]
	v_exp_f32_e32 v70, v70
	v_mfma_f32_16x16x32_bf16 v[42:45], v[234:237], v[130:133], v[42:45]
	v_mfma_f32_16x16x32_bf16 v[46:49], v[234:237], v[138:141], v[46:49]
	v_exp_f32_e32 v71, v71
	ds_read_b64_tr_b16 v[222:223], v180 offset:8704
	ds_read_b64_tr_b16 v[224:225], v180 offset:12800
	ds_read_b64_tr_b16 v[226:227], v181 offset:8704
	ds_read_b64_tr_b16 v[228:229], v181 offset:12800
	s_waitcnt lgkmcnt(8)
	v_mfma_f32_16x16x32_bf16 v[50:53], v[238:241], v[130:133], v[50:53]
	v_mfma_f32_16x16x32_bf16 v[54:57], v[238:241], v[138:141], v[54:57]
	v_exp_f32_e32 v72, v72
	v_mfma_f32_16x16x32_bf16 v[58:61], v[242:245], v[130:133], v[58:61]
	v_mfma_f32_16x16x32_bf16 v[62:65], v[242:245], v[138:141], v[62:65]
	v_exp_f32_e32 v73, v73
	v_mfma_f32_16x16x32_bf16 v[252:255], v[194:197], v[138:141], v[252:255]
	ds_read_b64_tr_b16 v[230:231], v180 offset:9216
	ds_read_b64_tr_b16 v[232:233], v180 offset:13312
	ds_read_b64_tr_b16 v[234:235], v181 offset:9216
	ds_read_b64_tr_b16 v[236:237], v181 offset:13312
	s_waitcnt lgkmcnt(8)
	v_mfma_f32_16x16x32_bf16 v[2:5], v[214:217], v[134:137], v[2:5]
	v_exp_f32_e32 v74, v74
	v_mfma_f32_16x16x32_bf16 v[6:9], v[214:217], v[142:145], v[6:9]
	v_cvt_pk_bf16_f32 v130, v66, v67
	v_mfma_f32_16x16x32_bf16 v[10:13], v[218:221], v[134:137], v[10:13]
	v_exp_f32_e32 v75, v75
	v_mfma_f32_16x16x32_bf16 v[14:17], v[218:221], v[142:145], v[14:17]
	v_cvt_pk_bf16_f32 v131, v68, v69
	ds_read_b64_tr_b16 v[238:239], v180 offset:9728
	ds_read_b64_tr_b16 v[240:241], v180 offset:13824
	ds_read_b64_tr_b16 v[242:243], v181 offset:9728
	ds_read_b64_tr_b16 v[244:245], v181 offset:13824
	s_waitcnt lgkmcnt(8)
	v_mfma_f32_16x16x32_bf16 v[18:21], v[222:225], v[134:137], v[18:21]
	v_exp_f32_e32 v76, v76
	v_mfma_f32_16x16x32_bf16 v[22:25], v[222:225], v[142:145], v[22:25]
	v_cvt_pk_bf16_f32 v132, v74, v75
	v_mfma_f32_16x16x32_bf16 v[26:29], v[226:229], v[134:137], v[26:29]
	v_exp_f32_e32 v77, v77
	v_mfma_f32_16x16x32_bf16 v[30:33], v[226:229], v[142:145], v[30:33]
	v_cvt_pk_bf16_f32 v133, v76, v77
	v_mfma_f32_16x16x32_bf16 v[246:249], v[194:197], v[134:137], v[246:249]
	s_waitcnt lgkmcnt(4)
	v_mfma_f32_16x16x32_bf16 v[34:37], v[230:233], v[134:137], v[34:37]
	v_exp_f32_e32 v78, v78
	v_mfma_f32_16x16x32_bf16 v[38:41], v[230:233], v[142:145], v[38:41]
	v_cvt_pk_bf16_f32 v138, v70, v71
	v_mfma_f32_16x16x32_bf16 v[42:45], v[234:237], v[134:137], v[42:45]
	v_exp_f32_e32 v79, v79
	v_mfma_f32_16x16x32_bf16 v[46:49], v[234:237], v[142:145], v[46:49]
	v_cvt_pk_bf16_f32 v139, v72, v73
	s_waitcnt lgkmcnt(0)
	v_mfma_f32_16x16x32_bf16 v[50:53], v[238:241], v[134:137], v[50:53]
	v_exp_f32_e32 v80, v80
	v_mfma_f32_16x16x32_bf16 v[54:57], v[238:241], v[142:145], v[54:57]
	v_cvt_pk_bf16_f32 v140, v78, v79
	v_mfma_f32_16x16x32_bf16 v[58:61], v[242:245], v[134:137], v[58:61]
	v_exp_f32_e32 v81, v81
	v_mfma_f32_16x16x32_bf16 v[62:65], v[242:245], v[142:145], v[62:65]
	v_cvt_pk_bf16_f32 v141, v80, v81
	v_mfma_f32_16x16x32_bf16 v[252:255], v[194:197], v[142:145], v[252:255]
	s_waitcnt vmcnt(0) lgkmcnt(0)
	s_barrier
	s_cmp_ge_u32 s97, 130
	s_cbranch_scc1 .Lf16_se_L2
	s_add_i32 m0, s96, 0x8000
	s_nop 0
	global_load_lds_dwordx4 v170, s[2:3]
	s_add_i32 m0, s96, 0xa000
	s_nop 0
	global_load_lds_dwordx4 v172, s[2:3]
	s_add_i32 m0, s96, 0xc000
	s_nop 0
	global_load_lds_dwordx4 v171, s[2:3]
	s_add_i32 m0, s96, 0xe000
	s_nop 0
	global_load_lds_dwordx4 v173, s[2:3]
	s_add_u32 s2, s2, 0x4000
	s_addc_u32 s3, s3, 0
.Lf16_se_L2:
	s_add_i32 s97, s97, 1
	s_cmp_lt_u32 s97, 132
	s_cbranch_scc0 .Lf16_done
	ds_read_b128 v[146:149], v183 offset:0
	ds_read_b128 v[150:153], v184 offset:0
	ds_read_b128 v[154:157], v185 offset:0
	ds_read_b128 v[158:161], v186 offset:0
	ds_read_b128 v[198:201], v183 offset:4096
	ds_read_b128 v[202:205], v184 offset:4096
	ds_read_b128 v[206:209], v185 offset:4096
	ds_read_b128 v[210:213], v186 offset:4096
	s_waitcnt lgkmcnt(6)
	v_mfma_f32_16x16x32_bf16 v[66:69], v[146:149], v[98:101], 0
	v_exp_f32_e32 v82, v82
	v_mfma_f32_16x16x32_bf16 v[70:73], v[146:149], v[114:117], 0
	v_exp_f32_e32 v83, v83
	v_mfma_f32_16x16x32_bf16 v[66:69], v[150:153], v[102:105], v[66:69]
	v_exp_f32_e32 v84, v84
	v_mfma_f32_16x16x32_bf16 v[70:73], v[150:153], v[118:121], v[70:73]
	v_exp_f32_e32 v85, v85
	ds_read_b128 v[146:149], v183 offset:8192
	ds_read_b128 v[150:153], v184 offset:8192
	s_waitcnt lgkmcnt(6)
	v_mfma_f32_16x16x32_bf16 v[66:69], v[154:157], v[106:109], v[66:69]
	v_exp_f32_e32 v86, v86
	v_mfma_f32_16x16x32_bf16 v[70:73], v[154:157], v[122:125], v[70:73]
	v_exp_f32_e32 v87, v87
	v_mfma_f32_16x16x32_bf16 v[66:69], v[158:161], v[110:113], v[66:69]
	v_exp_f32_e32 v88, v88
	v_mfma_f32_16x16x32_bf16 v[70:73], v[158:161], v[126:129], v[70:73]
	v_exp_f32_e32 v89, v89
	ds_read_b128 v[154:157], v185 offset:8192
	ds_read_b128 v[158:161], v186 offset:8192
	s_waitcnt lgkmcnt(6)
	v_mfma_f32_16x16x32_bf16 v[74:77], v[198:201], v[98:101], 0
	v_exp_f32_e32 v90, v90
	v_mfma_f32_16x16x32_bf16 v[78:81], v[198:201], v[114:117], 0
	v_exp_f32_e32 v91, v91
	v_cvt_pk_bf16_f32 v134, v82, v83
	v_mfma_f32_16x16x32_bf16 v[74:77], v[202:205], v[102:105], v[74:77]
	v_exp_f32_e32 v92, v92
	v_cvt_pk_bf16_f32 v135, v84, v85
	v_mfma_f32_16x16x32_bf16 v[78:81], v[202:205], v[118:121], v[78:81]
	v_exp_f32_e32 v93, v93
	v_cvt_pk_bf16_f32 v142, v86, v87
	ds_read_b128 v[198:201], v183 offset:12288
	ds_read_b128 v[202:205], v184 offset:12288
	s_waitcnt lgkmcnt(6)
; #define SBAR() __builtin_amdgcn_sched_barrier(0)
; #define RESC(a) do { if (__any((a) < 1.f)) { if (hi == 0) al_l[r32] = (a); asm volatile("s_waitcnt lgkmcnt(0)" ::: "memory"); \
;     for (int d = 0; d < 4; ++d) for (int r = 0; r < 16; ++r) o[d][r] *= al_l[crow(r, hi)]; } } while (0)
; #define RESC(a) do { if (__any((a) < 1.f)) { if (hi == 0) al_l[r32] = (a); asm volatile("s_waitcnt lgkmcnt(0)" ::: "memory"); \
;     for (int d = 0; d < 4; ++d) for (int r = 0; r < 16; ++r) o[d][r] *= al_l[crow(r, hi)]; } } while (0)
; #define ATT_SYNC(jn) do { ATT_WAIT_BAR(); if ((jn) < NT) ATT_DMA((jn), (jn) & 3); } while (0)
; __device__ __forceinline__ void attn_dma_body(const bf16_t* __restrict__ Qb, int ldq, int tpos0, const float* __restrict__ rope, const float* __restrict__ qgain, ...
;     ...
;   for (int j = 1; j + 1 < NT; j += 2) {
;     { SBAR(); qkt(pB0, pB1, (const bf16_t*)(lds + (j & 3) * SHM_SLOT), qr, r32, hi);
;       finishSM(pA0, pA1, alA, l_reg, pa0, pa1, pa2, pa3); s16x4 va[8]; pv_rd<0>(va, vb0 + ((j - 1) & 3) * (int)SHM_SLOT); SBAR();
;       if (!lead) ATT_SYNC(j + 2);
;       pv_d0_pre(o, vb0 + ((j - 1) & 3) * (int)SHM_SLOT, va, pa0, pa1, pa2, pa3); partialSM(pB0, pB1, m_reg, mnB, alB);
;       if (lead) ATT_SYNC(j + 2);
;       RESC(alB); }
;     { SBAR(); qkt(pA0, pA1, (const bf16_t*)(lds + ((j + 1) & 3) * SHM_SLOT), qr, r32, hi);
;       finishSM(pB0, pB1, alB, l_reg, pa0, pa1, pa2, pa3); s16x4 va[8]; pv_rd<0>(va, vb0 + (j & 3) * (int)SHM_SLOT); SBAR();
;       if (!lead) ATT_SYNC(j + 3);
;       pv_d0_pre(o, vb0 + (j & 3) * (int)SHM_SLOT, va, pa0, pa1, pa2, pa3); partialSM(pA0, pA1, m_reg, mnA, alA);
;       if (lead) ATT_SYNC(j + 3);
;       RESC(alA); }
;   }
	v_mfma_f32_16x16x32_bf16 v[74:77], v[206:209], v[106:109], v[74:77]
	v_exp_f32_e32 v94, v94
	v_cvt_pk_bf16_f32 v143, v88, v89
	v_mfma_f32_16x16x32_bf16 v[78:81], v[206:209], v[122:125], v[78:81]
	v_exp_f32_e32 v95, v95
	v_mfma_f32_16x16x32_bf16 v[74:77], v[210:213], v[110:113], v[74:77]
	v_exp_f32_e32 v96, v96
	v_mfma_f32_16x16x32_bf16 v[78:81], v[210:213], v[126:129], v[78:81]
	v_exp_f32_e32 v97, v97
	ds_read_b128 v[206:209], v185 offset:12288
	ds_read_b128 v[210:213], v186 offset:12288
	s_waitcnt lgkmcnt(6)
	v_mfma_f32_16x16x32_bf16 v[82:85], v[146:149], v[98:101], 0
	v_mfma_f32_16x16x32_bf16 v[86:89], v[146:149], v[114:117], 0
	v_cvt_pk_bf16_f32 v136, v90, v91
	v_mfma_f32_16x16x32_bf16 v[82:85], v[150:153], v[102:105], v[82:85]
	v_cvt_pk_bf16_f32 v137, v92, v93
	v_mfma_f32_16x16x32_bf16 v[86:89], v[150:153], v[118:121], v[86:89]
	v_cvt_pk_bf16_f32 v144, v94, v95
	s_waitcnt lgkmcnt(4)
	v_mfma_f32_16x16x32_bf16 v[82:85], v[154:157], v[106:109], v[82:85]
	v_cvt_pk_bf16_f32 v145, v96, v97
	v_mfma_f32_16x16x32_bf16 v[86:89], v[154:157], v[122:125], v[86:89]
	v_mfma_f32_16x16x32_bf16 v[82:85], v[158:161], v[110:113], v[82:85]
	v_mfma_f32_16x16x32_bf16 v[86:89], v[158:161], v[126:129], v[86:89]
	s_waitcnt lgkmcnt(2)
	v_mfma_f32_16x16x32_bf16 v[90:93], v[198:201], v[98:101], 0
	v_mfma_f32_16x16x32_bf16 v[94:97], v[198:201], v[114:117], 0
	v_mfma_f32_16x16x32_bf16 v[90:93], v[202:205], v[102:105], v[90:93]
	v_mfma_f32_16x16x32_bf16 v[94:97], v[202:205], v[118:121], v[94:97]
	ds_read_b64_tr_b16 v[214:215], v180 offset:32768
	ds_read_b64_tr_b16 v[216:217], v180 offset:36864
	ds_read_b64_tr_b16 v[218:219], v181 offset:32768
	ds_read_b64_tr_b16 v[220:221], v181 offset:36864
	ds_read_b64_tr_b16 v[222:223], v180 offset:33280
	ds_read_b64_tr_b16 v[224:225], v180 offset:37376
	ds_read_b64_tr_b16 v[226:227], v181 offset:33280
	ds_read_b64_tr_b16 v[228:229], v181 offset:37376
	ds_read_b64_tr_b16 v[230:231], v180 offset:33792
	ds_read_b64_tr_b16 v[232:233], v180 offset:37888
	ds_read_b64_tr_b16 v[234:235], v181 offset:33792
	ds_read_b64_tr_b16 v[236:237], v181 offset:37888
	s_waitcnt lgkmcnt(12)
	v_mfma_f32_16x16x32_bf16 v[90:93], v[206:209], v[106:109], v[90:93]
	v_mfma_f32_16x16x32_bf16 v[94:97], v[206:209], v[122:125], v[94:97]
	v_mfma_f32_16x16x32_bf16 v[90:93], v[210:213], v[110:113], v[90:93]
	v_mfma_f32_16x16x32_bf16 v[94:97], v[210:213], v[126:129], v[94:97]
	s_waitcnt lgkmcnt(8)
	v_mfma_f32_16x16x32_bf16 v[2:5], v[214:217], v[130:133], v[2:5]
	v_mfma_f32_16x16x32_bf16 v[6:9], v[214:217], v[138:141], v[6:9]
	v_exp_f32_e32 v66, v66
	v_mfma_f32_16x16x32_bf16 v[10:13], v[218:221], v[130:133], v[10:13]
	v_mfma_f32_16x16x32_bf16 v[14:17], v[218:221], v[138:141], v[14:17]
	v_exp_f32_e32 v67, v67
	ds_read_b64_tr_b16 v[238:239], v180 offset:34304
	ds_read_b64_tr_b16 v[240:241], v180 offset:38400
	ds_read_b64_tr_b16 v[242:243], v181 offset:34304
	ds_read_b64_tr_b16 v[244:245], v181 offset:38400
	s_waitcnt lgkmcnt(8)
	v_mfma_f32_16x16x32_bf16 v[18:21], v[222:225], v[130:133], v[18:21]
	v_mfma_f32_16x16x32_bf16 v[22:25], v[222:225], v[138:141], v[22:25]
	v_exp_f32_e32 v68, v68
	v_mfma_f32_16x16x32_bf16 v[26:29], v[226:229], v[130:133], v[26:29]
	v_mfma_f32_16x16x32_bf16 v[30:33], v[226:229], v[138:141], v[30:33]
	v_exp_f32_e32 v69, v69
	v_mfma_f32_16x16x32_bf16 v[246:249], v[194:197], v[130:133], v[246:249]
	ds_read_b64_tr_b16 v[214:215], v180 offset:40960
	ds_read_b64_tr_b16 v[216:217], v180 offset:45056
	ds_read_b64_tr_b16 v[218:219], v181 offset:40960
	ds_read_b64_tr_b16 v[220:221], v181 offset:45056
	s_waitcnt lgkmcnt(8)
	v_mfma_f32_16x16x32_bf16 v[34:37], v[230:233], v[130:133], v[34:37]
	v_mfma_f32_16x16x32_bf16 v[38:41], v[230:233], v[138:141], v[38:41]
	v_exp_f32_e32 v70, v70
	v_mfma_f32_16x16x32_bf16 v[42:45], v[234:237], v[130:133], v[42:45]
	v_mfma_f32_16x16x32_bf16 v[46:49], v[234:237], v[138:141], v[46:49]
	v_exp_f32_e32 v71, v71
	ds_read_b64_tr_b16 v[222:223], v180 offset:41472
	ds_read_b64_tr_b16 v[224:225], v180 offset:45568
	ds_read_b64_tr_b16 v[226:227], v181 offset:41472
	ds_read_b64_tr_b16 v[228:229], v181 offset:45568
	s_waitcnt lgkmcnt(8)
	v_mfma_f32_16x16x32_bf16 v[50:53], v[238:241], v[130:133], v[50:53]
	v_mfma_f32_16x16x32_bf16 v[54:57], v[238:241], v[138:141], v[54:57]
	v_exp_f32_e32 v72, v72
	v_mfma_f32_16x16x32_bf16 v[58:61], v[242:245], v[130:133], v[58:61]
	v_mfma_f32_16x16x32_bf16 v[62:65], v[242:245], v[138:141], v[62:65]
	v_exp_f32_e32 v73, v73
	v_mfma_f32_16x16x32_bf16 v[252:255], v[194:197], v[138:141], v[252:255]
	ds_read_b64_tr_b16 v[230:231], v180 offset:41984
	ds_read_b64_tr_b16 v[232:233], v180 offset:46080
	ds_read_b64_tr_b16 v[234:235], v181 offset:41984
	ds_read_b64_tr_b16 v[236:237], v181 offset:46080
	s_waitcnt lgkmcnt(8)
	v_mfma_f32_16x16x32_bf16 v[2:5], v[214:217], v[134:137], v[2:5]
	v_exp_f32_e32 v74, v74
	v_mfma_f32_16x16x32_bf16 v[6:9], v[214:217], v[142:145], v[6:9]
	v_cvt_pk_bf16_f32 v130, v66, v67
	v_mfma_f32_16x16x32_bf16 v[10:13], v[218:221], v[134:137], v[10:13]
	v_exp_f32_e32 v75, v75
	v_mfma_f32_16x16x32_bf16 v[14:17], v[218:221], v[142:145], v[14:17]
	v_cvt_pk_bf16_f32 v131, v68, v69
	ds_read_b64_tr_b16 v[238:239], v180 offset:42496
	ds_read_b64_tr_b16 v[240:241], v180 offset:46592
	ds_read_b64_tr_b16 v[242:243], v181 offset:42496
	ds_read_b64_tr_b16 v[244:245], v181 offset:46592
	s_waitcnt lgkmcnt(8)
	v_mfma_f32_16x16x32_bf16 v[18:21], v[222:225], v[134:137], v[18:21]
	v_exp_f32_e32 v76, v76
	v_mfma_f32_16x16x32_bf16 v[22:25], v[222:225], v[142:145], v[22:25]
	v_cvt_pk_bf16_f32 v132, v74, v75
	v_mfma_f32_16x16x32_bf16 v[26:29], v[226:229], v[134:137], v[26:29]
	v_exp_f32_e32 v77, v77
	v_mfma_f32_16x16x32_bf16 v[30:33], v[226:229], v[142:145], v[30:33]
	v_cvt_pk_bf16_f32 v133, v76, v77
	v_mfma_f32_16x16x32_bf16 v[246:249], v[194:197], v[134:137], v[246:249]
	s_waitcnt lgkmcnt(4)
	v_mfma_f32_16x16x32_bf16 v[34:37], v[230:233], v[134:137], v[34:37]
	v_exp_f32_e32 v78, v78
	v_mfma_f32_16x16x32_bf16 v[38:41], v[230:233], v[142:145], v[38:41]
	v_cvt_pk_bf16_f32 v138, v70, v71
	v_mfma_f32_16x16x32_bf16 v[42:45], v[234:237], v[134:137], v[42:45]
	v_exp_f32_e32 v79, v79
	v_mfma_f32_16x16x32_bf16 v[46:49], v[234:237], v[142:145], v[46:49]
	v_cvt_pk_bf16_f32 v139, v72, v73
	s_waitcnt lgkmcnt(0)
	v_mfma_f32_16x16x32_bf16 v[50:53], v[238:241], v[134:137], v[50:53]
	v_exp_f32_e32 v80, v80
	v_mfma_f32_16x16x32_bf16 v[54:57], v[238:241], v[142:145], v[54:57]
	v_cvt_pk_bf16_f32 v140, v78, v79
	v_mfma_f32_16x16x32_bf16 v[58:61], v[242:245], v[134:137], v[58:61]
	v_exp_f32_e32 v81, v81
	v_mfma_f32_16x16x32_bf16 v[62:65], v[242:245], v[142:145], v[62:65]
	v_cvt_pk_bf16_f32 v141, v80, v81
	v_mfma_f32_16x16x32_bf16 v[252:255], v[194:197], v[142:145], v[252:255]
	s_waitcnt vmcnt(0) lgkmcnt(0)
	s_barrier
; #define SBAR() __builtin_amdgcn_sched_barrier(0)
; #define RESC(a) do { if (__any((a) < 1.f)) { if (hi == 0) al_l[r32] = (a); asm volatile("s_waitcnt lgkmcnt(0)" ::: "memory"); \
;     for (int d = 0; d < 4; ++d) for (int r = 0; r < 16; ++r) o[d][r] *= al_l[crow(r, hi)]; } } while (0)
; #define RESC(a) do { if (__any((a) < 1.f)) { if (hi == 0) al_l[r32] = (a); asm volatile("s_waitcnt lgkmcnt(0)" ::: "memory"); \
;     for (int d = 0; d < 4; ++d) for (int r = 0; r < 16; ++r) o[d][r] *= al_l[crow(r, hi)]; } } while (0)
; #define ATT_SYNC(jn) do { ATT_WAIT_BAR(); if ((jn) < NT) ATT_DMA((jn), (jn) & 3); } while (0)
; __device__ __forceinline__ void attn_dma_body(const bf16_t* __restrict__ Qb, int ldq, int tpos0, const float* __restrict__ rope, const float* __restrict__ qgain, ...
;     ...
;   for (int j = 1; j + 1 < NT; j += 2) {
;     { SBAR(); qkt(pB0, pB1, (const bf16_t*)(lds + (j & 3) * SHM_SLOT), qr, r32, hi);
;       finishSM(pA0, pA1, alA, l_reg, pa0, pa1, pa2, pa3); s16x4 va[8]; pv_rd<0>(va, vb0 + ((j - 1) & 3) * (int)SHM_SLOT); SBAR();
;       if (!lead) ATT_SYNC(j + 2);
;       pv_d0_pre(o, vb0 + ((j - 1) & 3) * (int)SHM_SLOT, va, pa0, pa1, pa2, pa3); partialSM(pB0, pB1, m_reg, mnB, alB);
;       if (lead) ATT_SYNC(j + 2);
;       RESC(alB); }
;     { SBAR(); qkt(pA0, pA1, (const bf16_t*)(lds + ((j + 1) & 3) * SHM_SLOT), qr, r32, hi);
;       finishSM(pB0, pB1, alB, l_reg, pa0, pa1, pa2, pa3); s16x4 va[8]; pv_rd<0>(va, vb0 + (j & 3) * (int)SHM_SLOT); SBAR();
;       if (!lead) ATT_SYNC(j + 3);
;       pv_d0_pre(o, vb0 + (j & 3) * (int)SHM_SLOT, va, pa0, pa1, pa2, pa3); partialSM(pA0, pA1, m_reg, mnA, alA);
;       if (lead) ATT_SYNC(j + 3);
;       RESC(alA); }
;   }
	s_cmp_ge_u32 s97, 130
	s_cbranch_scc1 .Lf16_se_L3
	s_add_i32 m0, s96, 0x10000
	s_nop 0
	global_load_lds_dwordx4 v170, s[2:3]
	s_add_i32 m0, s96, 0x12000
	s_nop 0
	global_load_lds_dwordx4 v172, s[2:3]
	s_add_i32 m0, s96, 0x14000
	s_nop 0
	global_load_lds_dwordx4 v171, s[2:3]
	s_add_i32 m0, s96, 0x16000
	s_nop 0
	global_load_lds_dwordx4 v173, s[2:3]
	s_add_u32 s2, s2, 0x4000
	s_addc_u32 s3, s3, 0
.Lf16_se_L3:
	s_add_i32 s97, s97, 1
	s_branch .Lf16_L_loop
